# in-epilogue alignment barriers moved earlier (P5 after 1 group, P1 after 1st store, P6 after row-index setup) so the B half never waits for the A half
# speedup vs baseline: 1.0091x; 1.0091x over previous
; #define GAS __attribute__((address_space(1)))
; #define PG8_LAS __attribute__((address_space(3)))
; __device__ __forceinline__ unsigned cvt_pk_bf16(float lo, float hi) { const f32x2c v = {lo, hi}; const bf16x2c b = __builtin_convertvector(v, bf16x2c); return __builtin_bit_cast(unsigned, b); }
;     __device__ __forceinline__ void operator()(const i32x4 (&acc)[2][2][4][2], const Unit& u, int wr, int wc, int fr, int fq, PG8_LAS unsigned* scr) const {
;         const int row0 = u.pm * BM + wr * 64 + fr, col0 = u.pn * BM + wc * 32 + 8 * fq;
;         f32x4 cs[2][2];
; #pragma unroll
;         for (int bj = 0; bj < 2; ++bj)
; #pragma unroll
;             for (int n = 0; n < 2; ++n) cs[bj][n] = *(const PG8_LAS f32x4*)(scr + 256 + bj * HALF + wc * 32 + 8 * fq + 4 * n) * (1.0f / 127.0f);
; #pragma unroll
;         for (int ai = 0; ai < 2; ++ai)
; #pragma unroll
;             for (int m = 0; m < 4; ++m) { const int r = ai * HALF + wr * 64 + m * 16 + fr; const float rs = __uint_as_float(scr[r]); bf16_t* rowp = O + (size_t)(u.pm * BM + r) * ldc + col0;
; #pragma unroll
;                 for (int bj = 0; bj < 2; ++bj) { const f32x4 v0 = __builtin_convertvector(acc[ai][bj][m][0], f32x4) * (cs[bj][0] * rs), v1 = __builtin_convertvector(acc[ai][bj][m][1], f32x4) * (cs[bj][1] * rs);
;                     u32x4 w; w.x = cvt_pk_bf16(v0[0], v0[1]); w.y = cvt_pk_bf16(v0[2], v0[3]); w.z = cvt_pk_bf16(v1[0], v1[1]); w.w = cvt_pk_bf16(v1[2], v1[3]);
;                     *(GAS u32x4*)(rowp + bj * HALF) = w; } }
.LBB0_353:
	v_mov_b32_e32 v132, v164
	s_mov_b32 s42, 0x3c010204
	v_lshrrev_b32_e32 v128, 1, v132
	v_and_b32_e32 v152, 0x60, v128
	v_and_b32_e32 v153, 24, v128
	v_lshlrev_b32_e32 v128, 2, v152
	v_lshlrev_b32_e32 v129, 2, v153
	v_add3_u32 v138, s82, v128, v129
	ds_read_b128 v[128:131], v138
	v_and_b32_e32 v154, 15, v132
	v_ashrrev_i32_e32 v155, 2, v132
	ds_read_b128 v[132:135], v138 offset:16
	ds_read_b128 v[144:147], v138 offset:512
	ds_read_b128 v[148:151], v138 offset:528
	s_waitcnt lgkmcnt(3)
	v_pk_mul_f32 v[136:137], v[130:131], s[42:43] op_sel_hi:[1,0]
	v_pk_mul_f32 v[142:143], v[128:129], s[42:43] op_sel_hi:[1,0]
	s_waitcnt lgkmcnt(2)
	v_pk_mul_f32 v[138:139], v[134:135], s[42:43] op_sel_hi:[1,0]
	v_pk_mul_f32 v[140:141], v[132:133], s[42:43] op_sel_hi:[1,0]
	s_waitcnt lgkmcnt(1)
	v_pk_mul_f32 v[132:133], v[146:147], s[42:43] op_sel_hi:[1,0]
	v_pk_mul_f32 v[134:135], v[144:145], s[42:43] op_sel_hi:[1,0]
	s_waitcnt lgkmcnt(0)
	v_pk_mul_f32 v[128:129], v[150:151], s[42:43] op_sel_hi:[1,0]
	v_pk_mul_f32 v[130:131], v[148:149], s[42:43] op_sel_hi:[1,0]
	s_lshl_b32 s42, s70, 8
	v_or3_b32 v146, v152, s42, v153
	s_movk_i32 s42, 0xffc0
	v_and_or_b32 v158, v155, s42, v154
	v_lshl_add_u32 v151, v158, 2, s88
	ds_read2st64_b32 v[148:149], v151 offset1:2
	v_cvt_f32_i32_e32 v121, v121
	v_cvt_f32_i32_e32 v123, v123
	v_cvt_f32_i32_e32 v122, v122
	v_cvt_f32_i32_e32 v120, v120
	v_cvt_f32_i32_e32 v113, v113
	v_cvt_f32_i32_e32 v115, v115
	v_cvt_f32_i32_e32 v114, v114
	v_cvt_f32_i32_e32 v112, v112
	s_lshl_b32 s42, s69, 8
	s_waitcnt lgkmcnt(0)
	v_pk_mul_f32 v[154:155], v[136:137], v[148:149] op_sel_hi:[1,0]
	v_pk_mul_f32 v[156:157], v[142:143], v[148:149] op_sel_hi:[1,0]
	v_ashrrev_i32_e32 v147, 31, v146
	v_add_u32_e32 v150, s42, v158
	v_mov_b64_e32 v[144:145], s[22:23]
	v_pk_mul_f32 v[122:123], v[154:155], v[122:123]
	v_pk_mul_f32 v[120:121], v[156:157], v[120:121]
	v_pk_mul_f32 v[154:155], v[138:139], v[148:149] op_sel_hi:[1,0]
	v_pk_mul_f32 v[156:157], v[140:141], v[148:149] op_sel_hi:[1,0]
	v_mad_i64_i32 v[152:153], s[70:71], v150, s33, v[144:145]
	v_lshlrev_b64 v[146:147], 1, v[146:147]
	v_pk_mul_f32 v[154:155], v[154:155], v[114:115]
	v_pk_mul_f32 v[114:115], v[156:157], v[112:113]
	v_lshl_add_u64 v[152:153], v[152:153], 0, v[146:147]
	v_cvt_pk_bf16_f32 v112, v120, v121
	v_cvt_pk_bf16_f32 v113, v122, v123
	v_cvt_pk_bf16_f32 v114, v114, v115
	v_cvt_pk_bf16_f32 v115, v154, v155
	global_store_dwordx4 v[152:153], v[112:115], off
	s_and_b64 s[98:99], exec, s[44:45]
	s_cbranch_scc0 .Lp1_epi_nobar
	s_barrier
.Lp1_epi_nobar:
	v_cvt_f32_i32_e32 v117, v117
	v_cvt_f32_i32_e32 v119, v119
	v_cvt_f32_i32_e32 v113, v125
	v_cvt_f32_i32_e32 v115, v127
	v_cvt_f32_i32_e32 v114, v126
	v_cvt_f32_i32_e32 v112, v124
	v_cvt_f32_i32_e32 v118, v118
	v_cvt_f32_i32_e32 v116, v116
	v_pk_mul_f32 v[120:121], v[132:133], v[148:149] op_sel_hi:[1,0]
	v_pk_mul_f32 v[122:123], v[134:135], v[148:149] op_sel_hi:[1,0]
	v_pk_mul_f32 v[114:115], v[120:121], v[114:115]
	v_pk_mul_f32 v[112:113], v[122:123], v[112:113]
	v_pk_mul_f32 v[120:121], v[128:129], v[148:149] op_sel_hi:[1,0]
	v_pk_mul_f32 v[122:123], v[130:131], v[148:149] op_sel_hi:[1,0]
	v_pk_mul_f32 v[118:119], v[120:121], v[118:119]
	v_pk_mul_f32 v[116:117], v[122:123], v[116:117]
	v_cvt_pk_bf16_f32 v112, v112, v113
	v_cvt_pk_bf16_f32 v113, v114, v115
	v_cvt_pk_bf16_f32 v114, v116, v117
	v_cvt_pk_bf16_f32 v115, v118, v119
	global_store_dwordx4 v[152:153], v[112:115], off offset:256
	v_cvt_f32_i32_e32 v109, v109
	v_cvt_f32_i32_e32 v108, v108
	v_or_b32_e32 v112, 16, v158
	v_lshl_add_u32 v113, v112, 2, s88
	ds_read_b32 v114, v113
	v_cvt_f32_i32_e32 v111, v111
	v_cvt_f32_i32_e32 v110, v110
	v_cvt_f32_i32_e32 v89, v89
	v_cvt_f32_i32_e32 v91, v91
	v_cvt_f32_i32_e32 v90, v90
	v_cvt_f32_i32_e32 v88, v88
	v_or_b32_e32 v115, 32, v158
	s_waitcnt lgkmcnt(0)
	v_pk_mul_f32 v[122:123], v[136:137], v[114:115] op_sel_hi:[1,0]
	v_pk_mul_f32 v[124:125], v[142:143], v[114:115] op_sel_hi:[1,0]
	v_add_u32_e32 v112, s42, v112
	v_pk_mul_f32 v[110:111], v[122:123], v[110:111]
	v_pk_mul_f32 v[108:109], v[124:125], v[108:109]
	v_pk_mul_f32 v[122:123], v[138:139], v[114:115] op_sel_hi:[1,0]
	v_pk_mul_f32 v[124:125], v[140:141], v[114:115] op_sel_hi:[1,0]
	v_mad_i64_i32 v[112:113], s[70:71], v112, s33, v[144:145]
	v_pk_mul_f32 v[122:123], v[122:123], v[90:91]
	v_pk_mul_f32 v[90:91], v[124:125], v[88:89]
	v_lshl_add_u64 v[112:113], v[112:113], 0, v[146:147]
	v_lshl_add_u32 v116, v115, 2, s88
	v_or_b32_e32 v117, 48, v158
	v_cvt_pk_bf16_f32 v88, v108, v109
	v_cvt_pk_bf16_f32 v89, v110, v111
	v_cvt_pk_bf16_f32 v90, v90, v91
	v_cvt_pk_bf16_f32 v91, v122, v123
	v_lshl_add_u32 v119, v117, 2, s88
	ds_read_b32 v118, v116
	ds_read_b32 v116, v119
	ds_read_b32 v120, v151 offset:704
	global_store_dwordx4 v[112:113], v[88:91], off
	v_cvt_f32_i32_e32 v101, v101
	v_cvt_f32_i32_e32 v103, v103
	v_cvt_f32_i32_e32 v89, v105
	v_cvt_f32_i32_e32 v91, v107
	v_cvt_f32_i32_e32 v90, v106
	v_cvt_f32_i32_e32 v88, v104
	v_cvt_f32_i32_e32 v102, v102
	v_cvt_f32_i32_e32 v100, v100
	v_pk_mul_f32 v[104:105], v[132:133], v[114:115] op_sel_hi:[1,0]
	v_pk_mul_f32 v[106:107], v[134:135], v[114:115] op_sel_hi:[1,0]
	v_pk_mul_f32 v[90:91], v[104:105], v[90:91]
	v_pk_mul_f32 v[88:89], v[106:107], v[88:89]
	v_pk_mul_f32 v[104:105], v[128:129], v[114:115] op_sel_hi:[1,0]
	v_pk_mul_f32 v[106:107], v[130:131], v[114:115] op_sel_hi:[1,0]
	v_cvt_f32_i32_e32 v61, v61
	v_cvt_f32_i32_e32 v63, v63
	v_cvt_f32_i32_e32 v62, v62
	v_cvt_f32_i32_e32 v60, v60
	v_pk_mul_f32 v[102:103], v[104:105], v[102:103]
	v_pk_mul_f32 v[100:101], v[106:107], v[100:101]
	v_cvt_f32_i32_e32 v57, v57
	v_cvt_f32_i32_e32 v59, v59
	v_cvt_f32_i32_e32 v58, v58
	v_cvt_f32_i32_e32 v56, v56
	v_cvt_pk_bf16_f32 v88, v88, v89
	v_cvt_pk_bf16_f32 v89, v90, v91
	v_cvt_pk_bf16_f32 v90, v100, v101
	v_cvt_pk_bf16_f32 v91, v102, v103
	global_store_dwordx4 v[112:113], v[88:91], off offset:256
	s_waitcnt lgkmcnt(2)
; #define GAS __attribute__((address_space(1)))
; __device__ __forceinline__ unsigned cvt_pk_bf16(float lo, float hi) { const f32x2c v = {lo, hi}; const bf16x2c b = __builtin_convertvector(v, bf16x2c); return __builtin_bit_cast(unsigned, b); }
;     __device__ __forceinline__ void operator()(const i32x4 (&acc)[2][2][4][2], const Unit& u, int wr, int wc, int fr, int fq, PG8_LAS unsigned* scr) const {
;     ...
;             for (int m = 0; m < 4; ++m) { const int r = ai * HALF + wr * 64 + m * 16 + fr; const float rs = __uint_as_float(scr[r]); bf16_t* rowp = O + (size_t)(u.pm * BM + r) * ldc + col0;
; #pragma unroll
;                 for (int bj = 0; bj < 2; ++bj) { const f32x4 v0 = __builtin_convertvector(acc[ai][bj][m][0], f32x4) * (cs[bj][0] * rs), v1 = __builtin_convertvector(acc[ai][bj][m][1], f32x4) * (cs[bj][1] * rs);
;                     u32x4 w; w.x = cvt_pk_bf16(v0[0], v0[1]); w.y = cvt_pk_bf16(v0[2], v0[3]); w.z = cvt_pk_bf16(v1[0], v1[1]); w.w = cvt_pk_bf16(v1[2], v1[3]);
;                     *(GAS u32x4*)(rowp + bj * HALF) = w; } }
	v_pk_mul_f32 v[100:101], v[142:143], v[118:119] op_sel_hi:[1,0]
	v_cvt_f32_i32_e32 v29, v29
	v_pk_mul_f32 v[90:91], v[136:137], v[118:119] op_sel_hi:[1,0]
	v_add_u32_e32 v88, s42, v115
	v_pk_mul_f32 v[62:63], v[90:91], v[62:63]
	v_pk_mul_f32 v[60:61], v[100:101], v[60:61]
	v_pk_mul_f32 v[90:91], v[138:139], v[118:119] op_sel_hi:[1,0]
	v_pk_mul_f32 v[100:101], v[140:141], v[118:119] op_sel_hi:[1,0]
	v_mad_i64_i32 v[88:89], s[70:71], v88, s33, v[144:145]
	v_pk_mul_f32 v[90:91], v[90:91], v[58:59]
	v_pk_mul_f32 v[58:59], v[100:101], v[56:57]
	v_lshl_add_u64 v[88:89], v[88:89], 0, v[146:147]
	v_cvt_pk_bf16_f32 v56, v60, v61
	v_cvt_pk_bf16_f32 v57, v62, v63
	v_cvt_pk_bf16_f32 v58, v58, v59
	v_cvt_pk_bf16_f32 v59, v90, v91
	global_store_dwordx4 v[88:89], v[56:59], off
	v_pk_mul_f32 v[60:61], v[132:133], v[118:119] op_sel_hi:[1,0]
	v_pk_mul_f32 v[62:63], v[134:135], v[118:119] op_sel_hi:[1,0]
	v_cvt_f32_i32_e32 v57, v77
	v_cvt_f32_i32_e32 v59, v79
	v_cvt_f32_i32_e32 v58, v78
	v_cvt_f32_i32_e32 v56, v76
	v_cvt_f32_i32_e32 v31, v31
	v_cvt_f32_i32_e32 v30, v30
	v_pk_mul_f32 v[58:59], v[60:61], v[58:59]
	v_pk_mul_f32 v[56:57], v[62:63], v[56:57]
	v_cvt_f32_i32_e32 v61, v69
	v_cvt_f32_i32_e32 v63, v71
	v_cvt_f32_i32_e32 v62, v70
	v_cvt_f32_i32_e32 v60, v68
	v_pk_mul_f32 v[68:69], v[128:129], v[118:119] op_sel_hi:[1,0]
	v_pk_mul_f32 v[70:71], v[130:131], v[118:119] op_sel_hi:[1,0]
	v_cvt_f32_i32_e32 v28, v28
	v_pk_mul_f32 v[62:63], v[68:69], v[62:63]
	v_pk_mul_f32 v[60:61], v[70:71], v[60:61]
	v_cvt_f32_i32_e32 v25, v25
	v_cvt_f32_i32_e32 v27, v27
	v_cvt_f32_i32_e32 v26, v26
	v_cvt_f32_i32_e32 v24, v24
	v_cvt_pk_bf16_f32 v56, v56, v57
	v_cvt_pk_bf16_f32 v57, v58, v59
	v_cvt_pk_bf16_f32 v58, v60, v61
	v_cvt_pk_bf16_f32 v59, v62, v63
	global_store_dwordx4 v[88:89], v[56:59], off offset:256
	s_waitcnt lgkmcnt(1)
	v_pk_mul_f32 v[60:61], v[142:143], v[116:117] op_sel_hi:[1,0]
	v_cvt_f32_i32_e32 v21, v21
	v_pk_mul_f32 v[58:59], v[136:137], v[116:117] op_sel_hi:[1,0]
	v_add_u32_e32 v56, s42, v117
	v_pk_mul_f32 v[30:31], v[58:59], v[30:31]
	v_pk_mul_f32 v[28:29], v[60:61], v[28:29]
	v_pk_mul_f32 v[58:59], v[138:139], v[116:117] op_sel_hi:[1,0]
	v_pk_mul_f32 v[60:61], v[140:141], v[116:117] op_sel_hi:[1,0]
	v_mad_i64_i32 v[56:57], s[42:43], v56, s33, v[144:145]
	v_pk_mul_f32 v[58:59], v[58:59], v[26:27]
	v_pk_mul_f32 v[26:27], v[60:61], v[24:25]
	v_lshl_add_u64 v[56:57], v[56:57], 0, v[146:147]
	v_cvt_pk_bf16_f32 v24, v28, v29
	v_cvt_pk_bf16_f32 v25, v30, v31
	v_cvt_pk_bf16_f32 v26, v26, v27
	v_cvt_pk_bf16_f32 v27, v58, v59
	global_store_dwordx4 v[56:57], v[24:27], off
	v_pk_mul_f32 v[28:29], v[132:133], v[116:117] op_sel_hi:[1,0]
	v_pk_mul_f32 v[30:31], v[134:135], v[116:117] op_sel_hi:[1,0]
	v_cvt_f32_i32_e32 v25, v45
	v_cvt_f32_i32_e32 v27, v47
	v_cvt_f32_i32_e32 v26, v46
	v_cvt_f32_i32_e32 v24, v44
	v_cvt_f32_i32_e32 v20, v20
	v_cvt_f32_i32_e32 v23, v23
	v_pk_mul_f32 v[26:27], v[28:29], v[26:27]
	v_pk_mul_f32 v[24:25], v[30:31], v[24:25]
	v_cvt_f32_i32_e32 v29, v33
	v_cvt_f32_i32_e32 v31, v35
	v_cvt_f32_i32_e32 v30, v34
	v_cvt_f32_i32_e32 v28, v32
	v_pk_mul_f32 v[32:33], v[128:129], v[116:117] op_sel_hi:[1,0]
	v_pk_mul_f32 v[34:35], v[130:131], v[116:117] op_sel_hi:[1,0]
	v_pk_mul_f32 v[30:31], v[32:33], v[30:31]
	v_pk_mul_f32 v[28:29], v[34:35], v[28:29]
	v_cvt_pk_bf16_f32 v24, v24, v25
	v_cvt_pk_bf16_f32 v25, v26, v27
	v_cvt_pk_bf16_f32 v26, v28, v29
	v_cvt_pk_bf16_f32 v27, v30, v31
	global_store_dwordx4 v[56:57], v[24:27], off offset:256
	v_mov_b32_e32 v30, v149
	v_pk_mul_f32 v[32:33], v[136:137], v[30:31] op_sel_hi:[1,0]
	v_add_u32_e32 v24, 0x80, v150
	v_mad_i64_i32 v[24:25], s[42:43], v24, s33, v[144:145]
	v_lshl_add_u64 v[28:29], v[24:25], 0, v[146:147]
	v_cvt_f32_i32_e32 v25, v85
	v_cvt_f32_i32_e32 v24, v84
	v_cvt_f32_i32_e32 v27, v87
	v_cvt_f32_i32_e32 v26, v86
	v_pk_mul_f32 v[34:35], v[142:143], v[30:31] op_sel_hi:[1,0]
	v_pk_mul_f32 v[44:45], v[138:139], v[30:31] op_sel_hi:[1,0]
	v_pk_mul_f32 v[24:25], v[34:35], v[24:25]
	v_pk_mul_f32 v[26:27], v[32:33], v[26:27]
	v_cvt_f32_i32_e32 v33, v81
	v_cvt_f32_i32_e32 v35, v83
	v_cvt_f32_i32_e32 v34, v82
	v_cvt_f32_i32_e32 v32, v80
	v_pk_mul_f32 v[46:47], v[140:141], v[30:31] op_sel_hi:[1,0]
	v_cvt_pk_bf16_f32 v24, v24, v25
	v_pk_mul_f32 v[34:35], v[44:45], v[34:35]
	v_pk_mul_f32 v[32:33], v[46:47], v[32:33]
	v_cvt_pk_bf16_f32 v25, v26, v27
	v_cvt_pk_bf16_f32 v26, v32, v33
	v_cvt_pk_bf16_f32 v27, v34, v35
	global_store_dwordx4 v[28:29], v[24:27], off
	v_pk_mul_f32 v[32:33], v[132:133], v[30:31] op_sel_hi:[1,0]
	v_pk_mul_f32 v[34:35], v[134:135], v[30:31] op_sel_hi:[1,0]
	v_cvt_f32_i32_e32 v25, v97
	v_cvt_f32_i32_e32 v27, v99
	v_cvt_f32_i32_e32 v26, v98
	v_cvt_f32_i32_e32 v24, v96
	v_pk_mul_f32 v[44:45], v[128:129], v[30:31] op_sel_hi:[1,0]
	v_pk_mul_f32 v[30:31], v[130:131], v[30:31] op_sel_hi:[1,0]
	v_pk_mul_f32 v[26:27], v[32:33], v[26:27]
	v_pk_mul_f32 v[24:25], v[34:35], v[24:25]
	v_cvt_f32_i32_e32 v33, v93
	v_cvt_f32_i32_e32 v35, v95
	v_cvt_f32_i32_e32 v34, v94
	v_cvt_f32_i32_e32 v32, v92
	v_cvt_pk_bf16_f32 v24, v24, v25
	v_cvt_pk_bf16_f32 v25, v26, v27
	v_pk_mul_f32 v[34:35], v[44:45], v[34:35]
	v_pk_mul_f32 v[30:31], v[30:31], v[32:33]
	v_cvt_pk_bf16_f32 v27, v34, v35
	v_cvt_pk_bf16_f32 v26, v30, v31
	global_store_dwordx4 v[28:29], v[24:27], off offset:256
	ds_read2_b32 v[28:29], v151 offset0:144 offset1:160
	v_cvt_f32_i32_e32 v22, v22
	v_add_u32_e32 v24, 0x90, v150
	v_mad_i64_i32 v[24:25], s[42:43], v24, s33, v[144:145]
	v_lshl_add_u64 v[30:31], v[24:25], 0, v[146:147]
	v_cvt_f32_i32_e32 v25, v53
	v_cvt_f32_i32_e32 v27, v55
	v_cvt_f32_i32_e32 v26, v54
	v_cvt_f32_i32_e32 v24, v52
	s_waitcnt lgkmcnt(0)
; #define GAS __attribute__((address_space(1)))
; __device__ __forceinline__ unsigned cvt_pk_bf16(float lo, float hi) { const f32x2c v = {lo, hi}; const bf16x2c b = __builtin_convertvector(v, bf16x2c); return __builtin_bit_cast(unsigned, b); }
; #define PG8_BAR __builtin_amdgcn_s_barrier()
;     __device__ __forceinline__ void operator()(const i32x4 (&acc)[2][2][4][2], const Unit& u, int wr, int wc, int fr, int fq, PG8_LAS unsigned* scr) const {
;     ...
;             for (int m = 0; m < 4; ++m) { const int r = ai * HALF + wr * 64 + m * 16 + fr; const float rs = __uint_as_float(scr[r]); bf16_t* rowp = O + (size_t)(u.pm * BM + r) * ldc + col0;
; #pragma unroll
;                 for (int bj = 0; bj < 2; ++bj) { const f32x4 v0 = __builtin_convertvector(acc[ai][bj][m][0], f32x4) * (cs[bj][0] * rs), v1 = __builtin_convertvector(acc[ai][bj][m][1], f32x4) * (cs[bj][1] * rs);
;                     u32x4 w; w.x = cvt_pk_bf16(v0[0], v0[1]); w.y = cvt_pk_bf16(v0[2], v0[3]); w.z = cvt_pk_bf16(v1[0], v1[1]); w.w = cvt_pk_bf16(v1[2], v1[3]);
;                     *(GAS u32x4*)(rowp + bj * HALF) = w; } }
; template <class Epi, class Sched, bool GATHER, int MODE>
; __device__ __forceinline__ void gemm_phase(PG8_LAS unsigned char* lds, PG8_LAS unsigned* scr, const Gemm g, const Sched& S, const Epi& E, int tid_in) {
;     ...
;         if (!has_next) break;
;         cur = nxt; cA = nA; cB = nB; ++ui;
;         if (GATHER) { const u32x4 nx = gather_read(cur); c0[0] = nx[0]; c0[1] = nx[1]; c1[0] = nx[2]; c1[1] = nx[3]; }
;         if (wr == 1) PG8_BAR;
	v_pk_mul_f32 v[32:33], v[136:137], v[28:29] op_sel_hi:[1,0]
	v_pk_mul_f32 v[34:35], v[142:143], v[28:29] op_sel_hi:[1,0]
	v_pk_mul_f32 v[26:27], v[32:33], v[26:27]
	v_pk_mul_f32 v[24:25], v[34:35], v[24:25]
	v_cvt_f32_i32_e32 v33, v49
	v_cvt_f32_i32_e32 v35, v51
	v_cvt_f32_i32_e32 v34, v50
	v_cvt_f32_i32_e32 v32, v48
	v_pk_mul_f32 v[44:45], v[138:139], v[28:29] op_sel_hi:[1,0]
	v_pk_mul_f32 v[46:47], v[140:141], v[28:29] op_sel_hi:[1,0]
	v_pk_mul_f32 v[34:35], v[44:45], v[34:35]
	v_pk_mul_f32 v[32:33], v[46:47], v[32:33]
	v_cvt_pk_bf16_f32 v24, v24, v25
	v_cvt_pk_bf16_f32 v25, v26, v27
	v_cvt_pk_bf16_f32 v26, v32, v33
	v_cvt_pk_bf16_f32 v27, v34, v35
	global_store_dwordx4 v[30:31], v[24:27], off
	v_pk_mul_f32 v[32:33], v[132:133], v[28:29] op_sel_hi:[1,0]
	v_pk_mul_f32 v[34:35], v[134:135], v[28:29] op_sel_hi:[1,0]
	v_cvt_f32_i32_e32 v25, v73
	v_cvt_f32_i32_e32 v27, v75
	v_cvt_f32_i32_e32 v26, v74
	v_cvt_f32_i32_e32 v24, v72
	v_pk_mul_f32 v[44:45], v[128:129], v[28:29] op_sel_hi:[1,0]
	v_pk_mul_f32 v[46:47], v[130:131], v[28:29] op_sel_hi:[1,0]
	v_pk_mul_f32 v[26:27], v[32:33], v[26:27]
	v_pk_mul_f32 v[24:25], v[34:35], v[24:25]
	v_cvt_f32_i32_e32 v33, v65
	v_cvt_f32_i32_e32 v35, v67
	v_cvt_f32_i32_e32 v34, v66
	v_cvt_f32_i32_e32 v32, v64
	v_cvt_pk_bf16_f32 v24, v24, v25
	v_cvt_pk_bf16_f32 v25, v26, v27
	v_pk_mul_f32 v[34:35], v[44:45], v[34:35]
	v_pk_mul_f32 v[32:33], v[46:47], v[32:33]
	v_cvt_pk_bf16_f32 v27, v34, v35
	v_cvt_pk_bf16_f32 v26, v32, v33
	v_cvt_f32_i32_e32 v17, v17
	v_cvt_f32_i32_e32 v19, v19
	v_cvt_f32_i32_e32 v18, v18
	v_cvt_f32_i32_e32 v16, v16
	global_store_dwordx4 v[30:31], v[24:27], off offset:256
	v_cvt_f32_i32_e32 v9, v9
	v_cvt_f32_i32_e32 v11, v11
	v_mov_b32_e32 v26, v29
	v_pk_mul_f32 v[28:29], v[136:137], v[26:27] op_sel_hi:[1,0]
	v_pk_mul_f32 v[30:31], v[142:143], v[26:27] op_sel_hi:[1,0]
	v_add_u32_e32 v24, 0xa0, v150
	v_pk_mul_f32 v[22:23], v[28:29], v[22:23]
	v_pk_mul_f32 v[20:21], v[30:31], v[20:21]
	v_pk_mul_f32 v[28:29], v[138:139], v[26:27] op_sel_hi:[1,0]
	v_pk_mul_f32 v[30:31], v[140:141], v[26:27] op_sel_hi:[1,0]
	v_mad_i64_i32 v[24:25], s[42:43], v24, s33, v[144:145]
	v_pk_mul_f32 v[28:29], v[28:29], v[18:19]
	v_pk_mul_f32 v[18:19], v[30:31], v[16:17]
	v_lshl_add_u64 v[24:25], v[24:25], 0, v[146:147]
	v_cvt_pk_bf16_f32 v16, v20, v21
	v_cvt_pk_bf16_f32 v17, v22, v23
	v_cvt_pk_bf16_f32 v18, v18, v19
	v_cvt_pk_bf16_f32 v19, v28, v29
	global_store_dwordx4 v[24:25], v[16:19], off
	v_pk_mul_f32 v[20:21], v[132:133], v[26:27] op_sel_hi:[1,0]
	v_pk_mul_f32 v[22:23], v[134:135], v[26:27] op_sel_hi:[1,0]
	v_cvt_f32_i32_e32 v17, v41
	v_cvt_f32_i32_e32 v19, v43
	v_cvt_f32_i32_e32 v18, v42
	v_cvt_f32_i32_e32 v16, v40
	v_pk_mul_f32 v[28:29], v[128:129], v[26:27] op_sel_hi:[1,0]
	v_pk_mul_f32 v[26:27], v[130:131], v[26:27] op_sel_hi:[1,0]
	v_pk_mul_f32 v[18:19], v[20:21], v[18:19]
	v_pk_mul_f32 v[16:17], v[22:23], v[16:17]
	v_cvt_f32_i32_e32 v21, v37
	v_cvt_f32_i32_e32 v23, v39
	v_cvt_f32_i32_e32 v22, v38
	v_cvt_f32_i32_e32 v20, v36
	v_cvt_f32_i32_e32 v10, v10
	v_cvt_f32_i32_e32 v8, v8
	v_pk_mul_f32 v[22:23], v[28:29], v[22:23]
	v_pk_mul_f32 v[20:21], v[26:27], v[20:21]
	v_cvt_f32_i32_e32 v1, v1
	v_cvt_f32_i32_e32 v3, v3
	v_cvt_f32_i32_e32 v2, v2
	v_cvt_f32_i32_e32 v0, v0
	v_cvt_pk_bf16_f32 v16, v16, v17
	v_cvt_pk_bf16_f32 v17, v18, v19
	v_cvt_pk_bf16_f32 v18, v20, v21
	v_cvt_pk_bf16_f32 v19, v22, v23
	global_store_dwordx4 v[24:25], v[16:19], off offset:256
	v_pk_mul_f32 v[20:21], v[142:143], v[120:121] op_sel_hi:[1,0]
	v_cvt_f32_i32_e32 v5, v5
	v_pk_mul_f32 v[18:19], v[136:137], v[120:121] op_sel_hi:[1,0]
	v_add_u32_e32 v16, 0xb0, v150
	v_pk_mul_f32 v[10:11], v[18:19], v[10:11]
	v_pk_mul_f32 v[8:9], v[20:21], v[8:9]
	v_pk_mul_f32 v[18:19], v[138:139], v[120:121] op_sel_hi:[1,0]
	v_pk_mul_f32 v[20:21], v[140:141], v[120:121] op_sel_hi:[1,0]
	v_mad_i64_i32 v[16:17], s[42:43], v16, s33, v[144:145]
	v_pk_mul_f32 v[18:19], v[18:19], v[2:3]
	v_pk_mul_f32 v[2:3], v[20:21], v[0:1]
	v_lshl_add_u64 v[16:17], v[16:17], 0, v[146:147]
	v_cvt_pk_bf16_f32 v0, v8, v9
	v_cvt_pk_bf16_f32 v1, v10, v11
	v_cvt_pk_bf16_f32 v2, v2, v3
	v_cvt_pk_bf16_f32 v3, v18, v19
	global_store_dwordx4 v[16:17], v[0:3], off
	v_cvt_f32_i32_e32 v7, v7
	v_cvt_f32_i32_e32 v6, v6
	v_cvt_f32_i32_e32 v1, v13
	v_cvt_f32_i32_e32 v3, v15
	v_cvt_f32_i32_e32 v2, v14
	v_cvt_f32_i32_e32 v0, v12
	v_cvt_f32_i32_e32 v4, v4
	v_pk_mul_f32 v[8:9], v[132:133], v[120:121] op_sel_hi:[1,0]
	v_pk_mul_f32 v[10:11], v[134:135], v[120:121] op_sel_hi:[1,0]
	v_pk_mul_f32 v[2:3], v[8:9], v[2:3]
	v_pk_mul_f32 v[0:1], v[10:11], v[0:1]
	v_pk_mul_f32 v[8:9], v[128:129], v[120:121] op_sel_hi:[1,0]
	v_pk_mul_f32 v[10:11], v[130:131], v[120:121] op_sel_hi:[1,0]
	v_pk_mul_f32 v[6:7], v[8:9], v[6:7]
	v_pk_mul_f32 v[4:5], v[10:11], v[4:5]
	v_cvt_pk_bf16_f32 v0, v0, v1
	v_cvt_pk_bf16_f32 v1, v2, v3
	v_cvt_pk_bf16_f32 v2, v4, v5
	v_cvt_pk_bf16_f32 v3, v6, v7
	s_andn2_b64 vcc, exec, s[36:37]
	s_mov_b64 s[36:37], -1
	global_store_dwordx4 v[16:17], v[0:3], off offset:256
	s_cbranch_vccnz .LBB0_336
	s_andn2_b64 vcc, exec, s[10:11]
	s_cbranch_vccnz .LBB0_335
	s_barrier
	s_branch .LBB0_335

; #define PG8_LAS __attribute__((address_space(3)))
;     __device__ __forceinline__ void operator()(const i32x4 (&acc)[2][2][4][2], const Unit& u, int wr, int wc, int fr, int fq, PG8_LAS unsigned* scr) const {
;         const int j = u.pn & 7;
;         const int row0 = u.pm * BM + wr * 64 + fr, c0 = j * 128 + wc * 32 + 8 * fq, cl = wc * 32 + 8 * fq;
;         f32x4 bgv[2], buv[2], csg[2], csu[2];
;         constexpr float C2 = 1.702f * 1.44269504f;
; #pragma unroll
;         for (int n = 0; n < 2; ++n) { bgv[n] = *(const PG8_LAS f32x4*)(scr + 512 + cl + 4 * n) * C2; buv[n] = *(const PG8_LAS f32x4*)(scr + 512 + 128 + cl + 4 * n);
;             csg[n] = *(const PG8_LAS f32x4*)(scr + 256 + cl + 4 * n) * (C2 / 127.0f); csu[n] = *(const PG8_LAS f32x4*)(scr + 256 + 128 + cl + 4 * n) * (1.0f / 127.0f); }
; #pragma unroll
;         for (int ai = 0; ai < 2; ++ai)
; #pragma unroll
;             for (int mp = 0; mp < 4; mp += 2) { unsigned wp[2][2];
; #pragma unroll
;                 for (int hm = 0; hm < 2; ++hm) { const int m = mp + hm; const int r = ai * HALF + wr * 64 + m * 16 + fr; const float rs = __uint_as_float(scr[r]); float o[8];
; #pragma unroll
;                     for (int n = 0; n < 2; ++n) { const f32x4 sgr = csg[n] * rs, sur = csu[n] * rs;
; #pragma unroll
;                         for (int q = 0; q < 4; ++q) { const float h = fminf(__builtin_fmaf((float)acc[ai][0][m][n][q], sgr[q], bgv[n][q]), 7.0f * C2), up = fminf(fmaxf(__builtin_fmaf((float)acc[ai][1][m][n][q], sur[q], buv[n][q]), -7.0f), 7.0f);
;                             const float sg = __builtin_amdgcn_rcpf(1.0f + __builtin_amdgcn_exp2f(-h)); o[4 * n + q] = __builtin_fmaf(up, ACT_SC / C2, ACT_SC / C2) * (h * sg); } }
;                     int w0 = __builtin_amdgcn_cvt_pk_fp8_f32(o[0], o[1], 0, false); w0 = __builtin_amdgcn_cvt_pk_fp8_f32(o[2], o[3], w0, true);
;                     int w1 = __builtin_amdgcn_cvt_pk_fp8_f32(o[4], o[5], 0, false); w1 = __builtin_amdgcn_cvt_pk_fp8_f32(o[6], o[7], w1, true);
;                     wp[hm][0] = (unsigned)w0; wp[hm][1] = (unsigned)w1; }
.LBB0_807:
	v_ashrrev_i32_e32 v185, 2, v168
	v_and_b32_e32 v185, 0xffffffc0, v185
	v_bfe_u32 v201, v168, 4, 2
	v_lshrrev_b32_e32 v208, 1, v168
	v_and_b32_e32 v208, 0x60, v208
	v_lshl_or_b32 v208, v201, 3, v208
	s_lshl_b32 s10, s39, 7
	s_and_b32 s10, s10, 0x380
	v_and_b32_e32 v201, 1, v201
	v_lshlrev_b32_e32 v207, 3, v201
	v_add_u32_e32 v206, s10, v208
	v_sub_u32_e32 v206, v206, v207
	v_mov_b32_e32 v207, 0
	v_lshlrev_b32_e32 v201, 4, v201
	v_lshlrev_b32_e32 v208, 2, v208
	v_readlane_b32 s10, v255, 5
	v_and_b32_e32 v160, 15, v168
	v_lshl_add_u32 v161, v185, 2, 0
	v_lshl_add_u32 v161, v160, 2, v161
	v_add_u32_e32 v161, s10, v161
	ds_read2_b32 v[152:153], v161 offset0:0 offset1:16
	ds_read2_b32 v[154:155], v161 offset0:32 offset1:48
	ds_read2_b32 v[156:157], v161 offset0:128 offset1:144
	ds_read2_b32 v[158:159], v161 offset0:160 offset1:176
	v_lshl_add_u32 v185, s40, 8, v185
	v_or_b32_e32 v185, v185, v160
	v_add_u32_e32 v185, v185, v201
	s_mov_b32 s100, 0x405083aa
	s_mov_b32 s101, 0x405083aa
	v_add_u32_e32 v160, 0x21100, v208
	ds_read_b128 v[136:139], v160
	v_add_u32_e32 v160, 0x21300, v208
	ds_read_b128 v[140:143], v160
	v_add_u32_e32 v160, 0x20d00, v208
	ds_read_b128 v[144:147], v160
	v_add_u32_e32 v160, 0x20f00, v208
	ds_read_b128 v[148:151], v160
	s_waitcnt lgkmcnt(0)
	v_mul_f32_e32 v136, 0x401d265f, v136
	v_mul_f32_e32 v137, 0x401d265f, v137
	v_mul_f32_e32 v138, 0x401d265f, v138
	v_mul_f32_e32 v139, 0x401d265f, v139
	v_mul_f32_e32 v144, 0x3c9e6325, v144
	v_mul_f32_e32 v145, 0x3c9e6325, v145
	v_mul_f32_e32 v146, 0x3c9e6325, v146
	v_mul_f32_e32 v147, 0x3c9e6325, v147
	v_mul_f32_e32 v148, 0x3c010204, v148
	v_mul_f32_e32 v149, 0x3c010204, v149
	v_mul_f32_e32 v150, 0x3c010204, v150
	v_mul_f32_e32 v151, 0x3c010204, v151
	v_cvt_f32_i32_e32 v128, v128
	v_cvt_f32_i32_e32 v129, v129
	v_cvt_f32_i32_e32 v130, v130
	v_cvt_f32_i32_e32 v131, v131
	v_cvt_f32_i32_e32 v132, v132
	v_cvt_f32_i32_e32 v133, v133
	v_cvt_f32_i32_e32 v134, v134
	v_cvt_f32_i32_e32 v135, v135
	v_pk_mul_f32 v[160:161], v[144:145], v[152:153] op_sel_hi:[1,0]
	v_pk_mul_f32 v[162:163], v[146:147], v[152:153] op_sel_hi:[1,0]
	v_pk_fma_f32 v[128:129], v[128:129], v[160:161], v[136:137]
	v_pk_fma_f32 v[130:131], v[130:131], v[162:163], v[138:139]
	v_pk_mul_f32 v[160:161], v[148:149], v[152:153] op_sel_hi:[1,0]
	v_pk_mul_f32 v[162:163], v[150:151], v[152:153] op_sel_hi:[1,0]
	v_min_f32_e32 v128, 0x41898193, v128
	v_min_f32_e32 v129, 0x41898193, v129
	v_min_f32_e32 v130, 0x41898193, v130
	v_min_f32_e32 v131, 0x41898193, v131
	v_pk_fma_f32 v[132:133], v[132:133], v[160:161], v[140:141]
	v_pk_fma_f32 v[134:135], v[134:135], v[162:163], v[142:143]
	v_exp_f32_e64 v160, -v128
	v_exp_f32_e64 v161, -v129
	v_exp_f32_e64 v162, -v130
	v_exp_f32_e64 v163, -v131
	v_med3_f32 v132, v132, s8, v199
	v_med3_f32 v133, v133, s8, v199
	v_med3_f32 v134, v134, s8, v199
	v_med3_f32 v135, v135, s8, v199
	v_pk_add_f32 v[160:161], v[160:161], 1.0 op_sel_hi:[1,0]
	v_pk_add_f32 v[162:163], v[162:163], 1.0 op_sel_hi:[1,0]
	v_pk_fma_f32 v[132:133], v[132:133], s[100:101], s[100:101]
	v_pk_fma_f32 v[134:135], v[134:135], s[100:101], s[100:101]
	v_rcp_f32_e32 v160, v160
	v_rcp_f32_e32 v161, v161
	v_rcp_f32_e32 v162, v162
	v_rcp_f32_e32 v163, v163
	v_nop
	v_pk_mul_f32 v[128:129], v[128:129], v[160:161]
	v_pk_mul_f32 v[130:131], v[130:131], v[162:163]
	v_pk_mul_f32 v[128:129], v[132:133], v[128:129]
	v_pk_mul_f32 v[130:131], v[134:135], v[130:131]
	v_cvt_pk_fp8_f32 v128, v128, v129
	v_cvt_pk_fp8_f32 v128, v130, v131 op_sel:[0,0,1]
	s_and_b64 vcc, exec, s[62:63]
	s_cbranch_vccz .Lp5_epi_nobar
	s_barrier
.Lp5_epi_nobar:
	v_cvt_f32_i32_e32 v112, v112
	v_cvt_f32_i32_e32 v113, v113
	v_cvt_f32_i32_e32 v114, v114
	v_cvt_f32_i32_e32 v115, v115
	v_cvt_f32_i32_e32 v116, v116
	v_cvt_f32_i32_e32 v117, v117
	v_cvt_f32_i32_e32 v118, v118
	v_cvt_f32_i32_e32 v119, v119
	v_pk_mul_f32 v[202:203], v[144:145], v[152:153] op_sel:[0,1] op_sel_hi:[1,1]
	v_pk_mul_f32 v[204:205], v[146:147], v[152:153] op_sel:[0,1] op_sel_hi:[1,1]
	v_pk_fma_f32 v[112:113], v[112:113], v[202:203], v[136:137]
	v_pk_fma_f32 v[114:115], v[114:115], v[204:205], v[138:139]
	v_pk_mul_f32 v[202:203], v[148:149], v[152:153] op_sel:[0,1] op_sel_hi:[1,1]
	v_pk_mul_f32 v[204:205], v[150:151], v[152:153] op_sel:[0,1] op_sel_hi:[1,1]
	v_min_f32_e32 v112, 0x41898193, v112
	v_min_f32_e32 v113, 0x41898193, v113
	v_min_f32_e32 v114, 0x41898193, v114
	v_min_f32_e32 v115, 0x41898193, v115
	v_pk_fma_f32 v[116:117], v[116:117], v[202:203], v[140:141]
	v_pk_fma_f32 v[118:119], v[118:119], v[204:205], v[142:143]
	v_exp_f32_e64 v202, -v112
	v_exp_f32_e64 v203, -v113
	v_exp_f32_e64 v204, -v114
	v_exp_f32_e64 v205, -v115
	v_med3_f32 v116, v116, s8, v199
	v_med3_f32 v117, v117, s8, v199
	v_med3_f32 v118, v118, s8, v199
	v_med3_f32 v119, v119, s8, v199
	v_pk_add_f32 v[202:203], v[202:203], 1.0 op_sel_hi:[1,0]
	v_pk_add_f32 v[204:205], v[204:205], 1.0 op_sel_hi:[1,0]
	v_pk_fma_f32 v[116:117], v[116:117], s[100:101], s[100:101]
	v_pk_fma_f32 v[118:119], v[118:119], s[100:101], s[100:101]
	v_rcp_f32_e32 v202, v202
	v_rcp_f32_e32 v203, v203
	v_rcp_f32_e32 v204, v204
	v_rcp_f32_e32 v205, v205
	v_nop
	v_pk_mul_f32 v[112:113], v[112:113], v[202:203]
	v_pk_mul_f32 v[114:115], v[114:115], v[204:205]
	v_pk_mul_f32 v[112:113], v[116:117], v[112:113]
	v_pk_mul_f32 v[114:115], v[118:119], v[114:115]
	v_cvt_pk_fp8_f32 v130, v112, v113
	v_cvt_pk_fp8_f32 v130, v114, v115 op_sel:[0,0,1]
	v_cvt_f32_i32_e32 v96, v96
	v_cvt_f32_i32_e32 v97, v97
	v_cvt_f32_i32_e32 v98, v98
	v_cvt_f32_i32_e32 v99, v99
	v_cvt_f32_i32_e32 v100, v100
	v_cvt_f32_i32_e32 v101, v101
	v_cvt_f32_i32_e32 v102, v102
	v_cvt_f32_i32_e32 v103, v103
;     __device__ __forceinline__ void operator()(const i32x4 (&acc)[2][2][4][2], const Unit& u, int wr, int wc, int fr, int fq, PG8_LAS unsigned* scr) const {
;     ...
;                 for (int hm = 0; hm < 2; ++hm) { const int m = mp + hm; const int r = ai * HALF + wr * 64 + m * 16 + fr; const float rs = __uint_as_float(scr[r]); float o[8];
; #pragma unroll
;                     for (int n = 0; n < 2; ++n) { const f32x4 sgr = csg[n] * rs, sur = csu[n] * rs;
; #pragma unroll
;                         for (int q = 0; q < 4; ++q) { const float h = fminf(__builtin_fmaf((float)acc[ai][0][m][n][q], sgr[q], bgv[n][q]), 7.0f * C2), up = fminf(fmaxf(__builtin_fmaf((float)acc[ai][1][m][n][q], sur[q], buv[n][q]), -7.0f), 7.0f);
;                             const float sg = __builtin_amdgcn_rcpf(1.0f + __builtin_amdgcn_exp2f(-h)); o[4 * n + q] = __builtin_fmaf(up, ACT_SC / C2, ACT_SC / C2) * (h * sg); } }
;                     int w0 = __builtin_amdgcn_cvt_pk_fp8_f32(o[0], o[1], 0, false); w0 = __builtin_amdgcn_cvt_pk_fp8_f32(o[2], o[3], w0, true);
;                     int w1 = __builtin_amdgcn_cvt_pk_fp8_f32(o[4], o[5], 0, false); w1 = __builtin_amdgcn_cvt_pk_fp8_f32(o[6], o[7], w1, true);
;                     wp[hm][0] = (unsigned)w0; wp[hm][1] = (unsigned)w1; }
	v_pk_mul_f32 v[160:161], v[144:145], v[154:155] op_sel_hi:[1,0]
	v_pk_mul_f32 v[162:163], v[146:147], v[154:155] op_sel_hi:[1,0]
	v_pk_fma_f32 v[96:97], v[96:97], v[160:161], v[136:137]
	v_pk_fma_f32 v[98:99], v[98:99], v[162:163], v[138:139]
	v_pk_mul_f32 v[160:161], v[148:149], v[154:155] op_sel_hi:[1,0]
	v_pk_mul_f32 v[162:163], v[150:151], v[154:155] op_sel_hi:[1,0]
	v_min_f32_e32 v96, 0x41898193, v96
	v_min_f32_e32 v97, 0x41898193, v97
	v_min_f32_e32 v98, 0x41898193, v98
	v_min_f32_e32 v99, 0x41898193, v99
	v_pk_fma_f32 v[100:101], v[100:101], v[160:161], v[140:141]
	v_pk_fma_f32 v[102:103], v[102:103], v[162:163], v[142:143]
	v_exp_f32_e64 v160, -v96
	v_exp_f32_e64 v161, -v97
	v_exp_f32_e64 v162, -v98
	v_exp_f32_e64 v163, -v99
	v_med3_f32 v100, v100, s8, v199
	v_med3_f32 v101, v101, s8, v199
	v_med3_f32 v102, v102, s8, v199
	v_med3_f32 v103, v103, s8, v199
	v_pk_add_f32 v[160:161], v[160:161], 1.0 op_sel_hi:[1,0]
	v_pk_add_f32 v[162:163], v[162:163], 1.0 op_sel_hi:[1,0]
	v_pk_fma_f32 v[100:101], v[100:101], s[100:101], s[100:101]
	v_pk_fma_f32 v[102:103], v[102:103], s[100:101], s[100:101]
	v_rcp_f32_e32 v160, v160
	v_rcp_f32_e32 v161, v161
	v_rcp_f32_e32 v162, v162
	v_rcp_f32_e32 v163, v163
	v_nop
	v_pk_mul_f32 v[96:97], v[96:97], v[160:161]
	v_pk_mul_f32 v[98:99], v[98:99], v[162:163]
	v_pk_mul_f32 v[96:97], v[100:101], v[96:97]
	v_pk_mul_f32 v[98:99], v[102:103], v[98:99]
	v_cvt_pk_fp8_f32 v96, v96, v97
	v_cvt_pk_fp8_f32 v96, v98, v99 op_sel:[0,0,1]
	v_cvt_f32_i32_e32 v80, v80
	v_cvt_f32_i32_e32 v81, v81
	v_cvt_f32_i32_e32 v82, v82
	v_cvt_f32_i32_e32 v83, v83
	v_cvt_f32_i32_e32 v84, v84
	v_cvt_f32_i32_e32 v85, v85
	v_cvt_f32_i32_e32 v86, v86
	v_cvt_f32_i32_e32 v87, v87
	v_pk_mul_f32 v[202:203], v[144:145], v[154:155] op_sel:[0,1] op_sel_hi:[1,1]
	v_pk_mul_f32 v[204:205], v[146:147], v[154:155] op_sel:[0,1] op_sel_hi:[1,1]
	v_pk_fma_f32 v[80:81], v[80:81], v[202:203], v[136:137]
	v_pk_fma_f32 v[82:83], v[82:83], v[204:205], v[138:139]
	v_pk_mul_f32 v[202:203], v[148:149], v[154:155] op_sel:[0,1] op_sel_hi:[1,1]
	v_pk_mul_f32 v[204:205], v[150:151], v[154:155] op_sel:[0,1] op_sel_hi:[1,1]
	v_min_f32_e32 v80, 0x41898193, v80
	v_min_f32_e32 v81, 0x41898193, v81
	v_min_f32_e32 v82, 0x41898193, v82
	v_min_f32_e32 v83, 0x41898193, v83
	v_pk_fma_f32 v[84:85], v[84:85], v[202:203], v[140:141]
	v_pk_fma_f32 v[86:87], v[86:87], v[204:205], v[142:143]
	v_exp_f32_e64 v202, -v80
	v_exp_f32_e64 v203, -v81
	v_exp_f32_e64 v204, -v82
	v_exp_f32_e64 v205, -v83
	v_med3_f32 v84, v84, s8, v199
	v_med3_f32 v85, v85, s8, v199
	v_med3_f32 v86, v86, s8, v199
	v_med3_f32 v87, v87, s8, v199
	v_pk_add_f32 v[202:203], v[202:203], 1.0 op_sel_hi:[1,0]
	v_pk_add_f32 v[204:205], v[204:205], 1.0 op_sel_hi:[1,0]
	v_pk_fma_f32 v[84:85], v[84:85], s[100:101], s[100:101]
	v_pk_fma_f32 v[86:87], v[86:87], s[100:101], s[100:101]
	v_rcp_f32_e32 v202, v202
	v_rcp_f32_e32 v203, v203
	v_rcp_f32_e32 v204, v204
	v_rcp_f32_e32 v205, v205
	v_nop
	v_pk_mul_f32 v[80:81], v[80:81], v[202:203]
	v_pk_mul_f32 v[82:83], v[82:83], v[204:205]
	v_pk_mul_f32 v[80:81], v[84:85], v[80:81]
	v_pk_mul_f32 v[82:83], v[86:87], v[82:83]
	v_cvt_pk_fp8_f32 v98, v80, v81
	v_cvt_pk_fp8_f32 v98, v82, v83 op_sel:[0,0,1]
	v_cvt_f32_i32_e32 v64, v64
	v_cvt_f32_i32_e32 v65, v65
	v_cvt_f32_i32_e32 v66, v66
	v_cvt_f32_i32_e32 v67, v67
	v_cvt_f32_i32_e32 v68, v68
	v_cvt_f32_i32_e32 v69, v69
	v_cvt_f32_i32_e32 v70, v70
	v_cvt_f32_i32_e32 v71, v71
	v_pk_mul_f32 v[160:161], v[144:145], v[156:157] op_sel_hi:[1,0]
	v_pk_mul_f32 v[162:163], v[146:147], v[156:157] op_sel_hi:[1,0]
	v_pk_fma_f32 v[64:65], v[64:65], v[160:161], v[136:137]
	v_pk_fma_f32 v[66:67], v[66:67], v[162:163], v[138:139]
	v_pk_mul_f32 v[160:161], v[148:149], v[156:157] op_sel_hi:[1,0]
	v_pk_mul_f32 v[162:163], v[150:151], v[156:157] op_sel_hi:[1,0]
	v_min_f32_e32 v64, 0x41898193, v64
	v_min_f32_e32 v65, 0x41898193, v65
	v_min_f32_e32 v66, 0x41898193, v66
	v_min_f32_e32 v67, 0x41898193, v67
	v_pk_fma_f32 v[68:69], v[68:69], v[160:161], v[140:141]
	v_pk_fma_f32 v[70:71], v[70:71], v[162:163], v[142:143]
	v_exp_f32_e64 v160, -v64
	v_exp_f32_e64 v161, -v65
	v_exp_f32_e64 v162, -v66
	v_exp_f32_e64 v163, -v67
	v_med3_f32 v68, v68, s8, v199
	v_med3_f32 v69, v69, s8, v199
	v_med3_f32 v70, v70, s8, v199
	v_med3_f32 v71, v71, s8, v199
	v_pk_add_f32 v[160:161], v[160:161], 1.0 op_sel_hi:[1,0]
	v_pk_add_f32 v[162:163], v[162:163], 1.0 op_sel_hi:[1,0]
	v_pk_fma_f32 v[68:69], v[68:69], s[100:101], s[100:101]
	v_pk_fma_f32 v[70:71], v[70:71], s[100:101], s[100:101]
	v_rcp_f32_e32 v160, v160
	v_rcp_f32_e32 v161, v161
	v_rcp_f32_e32 v162, v162
	v_rcp_f32_e32 v163, v163
	v_nop
	v_pk_mul_f32 v[64:65], v[64:65], v[160:161]
	v_pk_mul_f32 v[66:67], v[66:67], v[162:163]
	v_pk_mul_f32 v[64:65], v[68:69], v[64:65]
	v_pk_mul_f32 v[66:67], v[70:71], v[66:67]
	v_cvt_pk_fp8_f32 v64, v64, v65
	v_cvt_pk_fp8_f32 v64, v66, v67 op_sel:[0,0,1]
	v_cvt_f32_i32_e32 v44, v44
	v_cvt_f32_i32_e32 v45, v45
	v_cvt_f32_i32_e32 v46, v46
	v_cvt_f32_i32_e32 v47, v47
	v_cvt_f32_i32_e32 v48, v48
	v_cvt_f32_i32_e32 v49, v49
	v_cvt_f32_i32_e32 v50, v50
	v_cvt_f32_i32_e32 v51, v51
	v_pk_mul_f32 v[202:203], v[144:145], v[156:157] op_sel:[0,1] op_sel_hi:[1,1]
	v_pk_mul_f32 v[204:205], v[146:147], v[156:157] op_sel:[0,1] op_sel_hi:[1,1]
	v_pk_fma_f32 v[44:45], v[44:45], v[202:203], v[136:137]
	v_pk_fma_f32 v[46:47], v[46:47], v[204:205], v[138:139]
	v_pk_mul_f32 v[202:203], v[148:149], v[156:157] op_sel:[0,1] op_sel_hi:[1,1]
	v_pk_mul_f32 v[204:205], v[150:151], v[156:157] op_sel:[0,1] op_sel_hi:[1,1]
	v_min_f32_e32 v44, 0x41898193, v44
	v_min_f32_e32 v45, 0x41898193, v45
	v_min_f32_e32 v46, 0x41898193, v46
; #define PG8_LAS __attribute__((address_space(3)))
;     __device__ __forceinline__ void operator()(const i32x4 (&acc)[2][2][4][2], const Unit& u, int wr, int wc, int fr, int fq, PG8_LAS unsigned* scr) const {
;     ...
;         for (int n = 0; n < 2; ++n) { bgv[n] = *(const PG8_LAS f32x4*)(scr + 512 + cl + 4 * n) * C2; buv[n] = *(const PG8_LAS f32x4*)(scr + 512 + 128 + cl + 4 * n);
;             csg[n] = *(const PG8_LAS f32x4*)(scr + 256 + cl + 4 * n) * (C2 / 127.0f); csu[n] = *(const PG8_LAS f32x4*)(scr + 256 + 128 + cl + 4 * n) * (1.0f / 127.0f); }
;     ...
;                 for (int hm = 0; hm < 2; ++hm) { const int m = mp + hm; const int r = ai * HALF + wr * 64 + m * 16 + fr; const float rs = __uint_as_float(scr[r]); float o[8];
; #pragma unroll
;                     for (int n = 0; n < 2; ++n) { const f32x4 sgr = csg[n] * rs, sur = csu[n] * rs;
; #pragma unroll
;                         for (int q = 0; q < 4; ++q) { const float h = fminf(__builtin_fmaf((float)acc[ai][0][m][n][q], sgr[q], bgv[n][q]), 7.0f * C2), up = fminf(fmaxf(__builtin_fmaf((float)acc[ai][1][m][n][q], sur[q], buv[n][q]), -7.0f), 7.0f);
;                             const float sg = __builtin_amdgcn_rcpf(1.0f + __builtin_amdgcn_exp2f(-h)); o[4 * n + q] = __builtin_fmaf(up, ACT_SC / C2, ACT_SC / C2) * (h * sg); } }
;                     int w0 = __builtin_amdgcn_cvt_pk_fp8_f32(o[0], o[1], 0, false); w0 = __builtin_amdgcn_cvt_pk_fp8_f32(o[2], o[3], w0, true);
;                     int w1 = __builtin_amdgcn_cvt_pk_fp8_f32(o[4], o[5], 0, false); w1 = __builtin_amdgcn_cvt_pk_fp8_f32(o[6], o[7], w1, true);
;                     wp[hm][0] = (unsigned)w0; wp[hm][1] = (unsigned)w1; }
	v_min_f32_e32 v47, 0x41898193, v47
	v_pk_fma_f32 v[48:49], v[48:49], v[202:203], v[140:141]
	v_pk_fma_f32 v[50:51], v[50:51], v[204:205], v[142:143]
	v_exp_f32_e64 v202, -v44
	v_exp_f32_e64 v203, -v45
	v_exp_f32_e64 v204, -v46
	v_exp_f32_e64 v205, -v47
	v_med3_f32 v48, v48, s8, v199
	v_med3_f32 v49, v49, s8, v199
	v_med3_f32 v50, v50, s8, v199
	v_med3_f32 v51, v51, s8, v199
	v_pk_add_f32 v[202:203], v[202:203], 1.0 op_sel_hi:[1,0]
	v_pk_add_f32 v[204:205], v[204:205], 1.0 op_sel_hi:[1,0]
	v_pk_fma_f32 v[48:49], v[48:49], s[100:101], s[100:101]
	v_pk_fma_f32 v[50:51], v[50:51], s[100:101], s[100:101]
	v_rcp_f32_e32 v202, v202
	v_rcp_f32_e32 v203, v203
	v_rcp_f32_e32 v204, v204
	v_rcp_f32_e32 v205, v205
	v_nop
	v_pk_mul_f32 v[44:45], v[44:45], v[202:203]
	v_pk_mul_f32 v[46:47], v[46:47], v[204:205]
	v_pk_mul_f32 v[44:45], v[48:49], v[44:45]
	v_pk_mul_f32 v[46:47], v[50:51], v[46:47]
	v_cvt_pk_fp8_f32 v66, v44, v45
	v_cvt_pk_fp8_f32 v66, v46, v47 op_sel:[0,0,1]
	v_cvt_f32_i32_e32 v24, v24
	v_cvt_f32_i32_e32 v25, v25
	v_cvt_f32_i32_e32 v26, v26
	v_cvt_f32_i32_e32 v27, v27
	v_cvt_f32_i32_e32 v28, v28
	v_cvt_f32_i32_e32 v29, v29
	v_cvt_f32_i32_e32 v30, v30
	v_cvt_f32_i32_e32 v31, v31
	v_pk_mul_f32 v[160:161], v[144:145], v[158:159] op_sel_hi:[1,0]
	v_pk_mul_f32 v[162:163], v[146:147], v[158:159] op_sel_hi:[1,0]
	v_pk_fma_f32 v[24:25], v[24:25], v[160:161], v[136:137]
	v_pk_fma_f32 v[26:27], v[26:27], v[162:163], v[138:139]
	v_pk_mul_f32 v[160:161], v[148:149], v[158:159] op_sel_hi:[1,0]
	v_pk_mul_f32 v[162:163], v[150:151], v[158:159] op_sel_hi:[1,0]
	v_min_f32_e32 v24, 0x41898193, v24
	v_min_f32_e32 v25, 0x41898193, v25
	v_min_f32_e32 v26, 0x41898193, v26
	v_min_f32_e32 v27, 0x41898193, v27
	v_pk_fma_f32 v[28:29], v[28:29], v[160:161], v[140:141]
	v_pk_fma_f32 v[30:31], v[30:31], v[162:163], v[142:143]
	v_exp_f32_e64 v160, -v24
	v_exp_f32_e64 v161, -v25
	v_exp_f32_e64 v162, -v26
	v_exp_f32_e64 v163, -v27
	v_med3_f32 v28, v28, s8, v199
	v_med3_f32 v29, v29, s8, v199
	v_med3_f32 v30, v30, s8, v199
	v_med3_f32 v31, v31, s8, v199
	v_pk_add_f32 v[160:161], v[160:161], 1.0 op_sel_hi:[1,0]
	v_pk_add_f32 v[162:163], v[162:163], 1.0 op_sel_hi:[1,0]
	v_pk_fma_f32 v[28:29], v[28:29], s[100:101], s[100:101]
	v_pk_fma_f32 v[30:31], v[30:31], s[100:101], s[100:101]
	v_rcp_f32_e32 v160, v160
	v_rcp_f32_e32 v161, v161
	v_rcp_f32_e32 v162, v162
	v_rcp_f32_e32 v163, v163
	v_nop
	v_pk_mul_f32 v[24:25], v[24:25], v[160:161]
	v_pk_mul_f32 v[26:27], v[26:27], v[162:163]
	v_pk_mul_f32 v[24:25], v[28:29], v[24:25]
	v_pk_mul_f32 v[26:27], v[30:31], v[26:27]
	v_cvt_pk_fp8_f32 v24, v24, v25
	v_cvt_pk_fp8_f32 v24, v26, v27 op_sel:[0,0,1]
	v_cvt_f32_i32_e32 v8, v8
	v_cvt_f32_i32_e32 v9, v9
	v_cvt_f32_i32_e32 v10, v10
	v_cvt_f32_i32_e32 v11, v11
	v_cvt_f32_i32_e32 v12, v12
	v_cvt_f32_i32_e32 v13, v13
	v_cvt_f32_i32_e32 v14, v14
	v_cvt_f32_i32_e32 v15, v15
	v_pk_mul_f32 v[202:203], v[144:145], v[158:159] op_sel:[0,1] op_sel_hi:[1,1]
	v_pk_mul_f32 v[204:205], v[146:147], v[158:159] op_sel:[0,1] op_sel_hi:[1,1]
	v_pk_fma_f32 v[8:9], v[8:9], v[202:203], v[136:137]
	v_pk_fma_f32 v[10:11], v[10:11], v[204:205], v[138:139]
	v_pk_mul_f32 v[202:203], v[148:149], v[158:159] op_sel:[0,1] op_sel_hi:[1,1]
	v_pk_mul_f32 v[204:205], v[150:151], v[158:159] op_sel:[0,1] op_sel_hi:[1,1]
	v_min_f32_e32 v8, 0x41898193, v8
	v_min_f32_e32 v9, 0x41898193, v9
	v_min_f32_e32 v10, 0x41898193, v10
	v_min_f32_e32 v11, 0x41898193, v11
	v_pk_fma_f32 v[12:13], v[12:13], v[202:203], v[140:141]
	v_pk_fma_f32 v[14:15], v[14:15], v[204:205], v[142:143]
	v_exp_f32_e64 v202, -v8
	v_exp_f32_e64 v203, -v9
	v_exp_f32_e64 v204, -v10
	v_exp_f32_e64 v205, -v11
	v_med3_f32 v12, v12, s8, v199
	v_med3_f32 v13, v13, s8, v199
	v_med3_f32 v14, v14, s8, v199
	v_med3_f32 v15, v15, s8, v199
	v_pk_add_f32 v[202:203], v[202:203], 1.0 op_sel_hi:[1,0]
	v_pk_add_f32 v[204:205], v[204:205], 1.0 op_sel_hi:[1,0]
	v_pk_fma_f32 v[12:13], v[12:13], s[100:101], s[100:101]
	v_pk_fma_f32 v[14:15], v[14:15], s[100:101], s[100:101]
	v_rcp_f32_e32 v202, v202
	v_rcp_f32_e32 v203, v203
	v_rcp_f32_e32 v204, v204
	v_rcp_f32_e32 v205, v205
	v_nop
	v_pk_mul_f32 v[8:9], v[8:9], v[202:203]
	v_pk_mul_f32 v[10:11], v[10:11], v[204:205]
	v_pk_mul_f32 v[8:9], v[12:13], v[8:9]
	v_pk_mul_f32 v[10:11], v[14:15], v[10:11]
	v_cvt_pk_fp8_f32 v26, v8, v9
	v_cvt_pk_fp8_f32 v26, v10, v11 op_sel:[0,0,1]
	v_add_u32_e32 v160, 0x21110, v208
	ds_read_b128 v[136:139], v160
	v_add_u32_e32 v160, 0x21310, v208
	ds_read_b128 v[140:143], v160
	v_add_u32_e32 v160, 0x20d10, v208
	ds_read_b128 v[144:147], v160
	v_add_u32_e32 v160, 0x20f10, v208
	ds_read_b128 v[148:151], v160
	s_waitcnt lgkmcnt(0)
; #define PG8_LAS __attribute__((address_space(3)))
;     __device__ __forceinline__ void operator()(const i32x4 (&acc)[2][2][4][2], const Unit& u, int wr, int wc, int fr, int fq, PG8_LAS unsigned* scr) const {
;         const int j = u.pn & 7;
;         const int row0 = u.pm * BM + wr * 64 + fr, c0 = j * 128 + wc * 32 + 8 * fq, cl = wc * 32 + 8 * fq;
;         f32x4 bgv[2], buv[2], csg[2], csu[2];
;         constexpr float C2 = 1.702f * 1.44269504f;
; #pragma unroll
;         for (int n = 0; n < 2; ++n) { bgv[n] = *(const PG8_LAS f32x4*)(scr + 512 + cl + 4 * n) * C2; buv[n] = *(const PG8_LAS f32x4*)(scr + 512 + 128 + cl + 4 * n);
;             csg[n] = *(const PG8_LAS f32x4*)(scr + 256 + cl + 4 * n) * (C2 / 127.0f); csu[n] = *(const PG8_LAS f32x4*)(scr + 256 + 128 + cl + 4 * n) * (1.0f / 127.0f); }
; #pragma unroll
;         for (int ai = 0; ai < 2; ++ai)
; #pragma unroll
;             for (int mp = 0; mp < 4; mp += 2) { unsigned wp[2][2];
; #pragma unroll
;                 for (int hm = 0; hm < 2; ++hm) { const int m = mp + hm; const int r = ai * HALF + wr * 64 + m * 16 + fr; const float rs = __uint_as_float(scr[r]); float o[8];
; #pragma unroll
;                     for (int n = 0; n < 2; ++n) { const f32x4 sgr = csg[n] * rs, sur = csu[n] * rs;
; #pragma unroll
;                         for (int q = 0; q < 4; ++q) { const float h = fminf(__builtin_fmaf((float)acc[ai][0][m][n][q], sgr[q], bgv[n][q]), 7.0f * C2), up = fminf(fmaxf(__builtin_fmaf((float)acc[ai][1][m][n][q], sur[q], buv[n][q]), -7.0f), 7.0f);
;                             const float sg = __builtin_amdgcn_rcpf(1.0f + __builtin_amdgcn_exp2f(-h)); o[4 * n + q] = __builtin_fmaf(up, ACT_SC / C2, ACT_SC / C2) * (h * sg); } }
;                     int w0 = __builtin_amdgcn_cvt_pk_fp8_f32(o[0], o[1], 0, false); w0 = __builtin_amdgcn_cvt_pk_fp8_f32(o[2], o[3], w0, true);
;                     int w1 = __builtin_amdgcn_cvt_pk_fp8_f32(o[4], o[5], 0, false); w1 = __builtin_amdgcn_cvt_pk_fp8_f32(o[6], o[7], w1, true);
;                     wp[hm][0] = (unsigned)w0; wp[hm][1] = (unsigned)w1; }
;                 { auto r0 = __builtin_amdgcn_permlane16_swap(wp[0][0], wp[1][0], false, false); wp[0][0] = r0[0]; wp[1][0] = r0[1];
;                   auto r1 = __builtin_amdgcn_permlane16_swap(wp[0][1], wp[1][1], false, false); wp[0][1] = r1[0]; wp[1][1] = r1[1]; }
;                 const int odd = fq & 1;
	v_mul_f32_e32 v136, 0x401d265f, v136
	v_mul_f32_e32 v137, 0x401d265f, v137
	v_mul_f32_e32 v138, 0x401d265f, v138
	v_mul_f32_e32 v139, 0x401d265f, v139
	v_mul_f32_e32 v144, 0x3c9e6325, v144
	v_mul_f32_e32 v145, 0x3c9e6325, v145
	v_mul_f32_e32 v146, 0x3c9e6325, v146
	v_mul_f32_e32 v147, 0x3c9e6325, v147
	v_mul_f32_e32 v148, 0x3c010204, v148
	v_mul_f32_e32 v149, 0x3c010204, v149
	v_mul_f32_e32 v150, 0x3c010204, v150
	v_mul_f32_e32 v151, 0x3c010204, v151
	v_cvt_f32_i32_e32 v120, v120
	v_cvt_f32_i32_e32 v121, v121
	v_cvt_f32_i32_e32 v122, v122
	v_cvt_f32_i32_e32 v123, v123
	v_cvt_f32_i32_e32 v124, v124
	v_cvt_f32_i32_e32 v125, v125
	v_cvt_f32_i32_e32 v126, v126
	v_cvt_f32_i32_e32 v127, v127
	v_pk_mul_f32 v[160:161], v[144:145], v[152:153] op_sel_hi:[1,0]
	v_pk_mul_f32 v[162:163], v[146:147], v[152:153] op_sel_hi:[1,0]
	v_pk_fma_f32 v[120:121], v[120:121], v[160:161], v[136:137]
	v_pk_fma_f32 v[122:123], v[122:123], v[162:163], v[138:139]
	v_pk_mul_f32 v[160:161], v[148:149], v[152:153] op_sel_hi:[1,0]
	v_pk_mul_f32 v[162:163], v[150:151], v[152:153] op_sel_hi:[1,0]
	v_min_f32_e32 v120, 0x41898193, v120
	v_min_f32_e32 v121, 0x41898193, v121
	v_min_f32_e32 v122, 0x41898193, v122
	v_min_f32_e32 v123, 0x41898193, v123
	v_pk_fma_f32 v[124:125], v[124:125], v[160:161], v[140:141]
	v_pk_fma_f32 v[126:127], v[126:127], v[162:163], v[142:143]
	v_exp_f32_e64 v160, -v120
	v_exp_f32_e64 v161, -v121
	v_exp_f32_e64 v162, -v122
	v_exp_f32_e64 v163, -v123
	v_med3_f32 v124, v124, s8, v199
	v_med3_f32 v125, v125, s8, v199
	v_med3_f32 v126, v126, s8, v199
	v_med3_f32 v127, v127, s8, v199
	v_pk_add_f32 v[160:161], v[160:161], 1.0 op_sel_hi:[1,0]
	v_pk_add_f32 v[162:163], v[162:163], 1.0 op_sel_hi:[1,0]
	v_pk_fma_f32 v[124:125], v[124:125], s[100:101], s[100:101]
	v_pk_fma_f32 v[126:127], v[126:127], s[100:101], s[100:101]
	v_rcp_f32_e32 v160, v160
	v_rcp_f32_e32 v161, v161
	v_rcp_f32_e32 v162, v162
	v_rcp_f32_e32 v163, v163
	v_nop
	v_pk_mul_f32 v[120:121], v[120:121], v[160:161]
	v_pk_mul_f32 v[122:123], v[122:123], v[162:163]
	v_pk_mul_f32 v[120:121], v[124:125], v[120:121]
	v_pk_mul_f32 v[122:123], v[126:127], v[122:123]
	v_cvt_pk_fp8_f32 v129, v120, v121
	v_cvt_pk_fp8_f32 v129, v122, v123 op_sel:[0,0,1]
	v_cvt_f32_i32_e32 v104, v104
	v_cvt_f32_i32_e32 v105, v105
	v_cvt_f32_i32_e32 v106, v106
	v_cvt_f32_i32_e32 v107, v107
	v_cvt_f32_i32_e32 v108, v108
	v_cvt_f32_i32_e32 v109, v109
	v_cvt_f32_i32_e32 v110, v110
	v_cvt_f32_i32_e32 v111, v111
	v_pk_mul_f32 v[202:203], v[144:145], v[152:153] op_sel:[0,1] op_sel_hi:[1,1]
	v_pk_mul_f32 v[204:205], v[146:147], v[152:153] op_sel:[0,1] op_sel_hi:[1,1]
	v_pk_fma_f32 v[104:105], v[104:105], v[202:203], v[136:137]
	v_pk_fma_f32 v[106:107], v[106:107], v[204:205], v[138:139]
	v_pk_mul_f32 v[202:203], v[148:149], v[152:153] op_sel:[0,1] op_sel_hi:[1,1]
	v_pk_mul_f32 v[204:205], v[150:151], v[152:153] op_sel:[0,1] op_sel_hi:[1,1]
	v_min_f32_e32 v104, 0x41898193, v104
	v_min_f32_e32 v105, 0x41898193, v105
	v_min_f32_e32 v106, 0x41898193, v106
	v_min_f32_e32 v107, 0x41898193, v107
	v_pk_fma_f32 v[108:109], v[108:109], v[202:203], v[140:141]
	v_pk_fma_f32 v[110:111], v[110:111], v[204:205], v[142:143]
	v_exp_f32_e64 v202, -v104
	v_exp_f32_e64 v203, -v105
	v_exp_f32_e64 v204, -v106
	v_exp_f32_e64 v205, -v107
	v_med3_f32 v108, v108, s8, v199
	v_med3_f32 v109, v109, s8, v199
	v_med3_f32 v110, v110, s8, v199
	v_med3_f32 v111, v111, s8, v199
	v_pk_add_f32 v[202:203], v[202:203], 1.0 op_sel_hi:[1,0]
	v_pk_add_f32 v[204:205], v[204:205], 1.0 op_sel_hi:[1,0]
	v_pk_fma_f32 v[108:109], v[108:109], s[100:101], s[100:101]
	v_pk_fma_f32 v[110:111], v[110:111], s[100:101], s[100:101]
	v_rcp_f32_e32 v202, v202
	v_rcp_f32_e32 v203, v203
	v_rcp_f32_e32 v204, v204
	v_rcp_f32_e32 v205, v205
	v_nop
	v_pk_mul_f32 v[104:105], v[104:105], v[202:203]
	v_pk_mul_f32 v[106:107], v[106:107], v[204:205]
	v_pk_mul_f32 v[104:105], v[108:109], v[104:105]
	v_pk_mul_f32 v[106:107], v[110:111], v[106:107]
	v_cvt_pk_fp8_f32 v131, v104, v105
	v_cvt_pk_fp8_f32 v131, v106, v107 op_sel:[0,0,1]
	s_nop 1
	v_permlane16_swap_b32_e32 v128, v130
	v_permlane16_swap_b32_e32 v129, v131
	v_add_u32_e32 v160, 0, v185
	v_mov_b32_e32 v161, 0
	v_lshlrev_b64 v[160:161], 10, v[160:161]
	v_lshl_add_u64 v[160:161], s[60:61], 0, v[160:161]
	v_lshl_add_u64 v[160:161], v[160:161], 0, v[206:207]
	global_store_dwordx4 v[160:161], v[128:131], off
	v_cvt_f32_i32_e32 v88, v88
	v_cvt_f32_i32_e32 v89, v89
	v_cvt_f32_i32_e32 v90, v90
	v_cvt_f32_i32_e32 v91, v91
	v_cvt_f32_i32_e32 v92, v92
	v_cvt_f32_i32_e32 v93, v93
	v_cvt_f32_i32_e32 v94, v94
	v_cvt_f32_i32_e32 v95, v95
	v_pk_mul_f32 v[160:161], v[144:145], v[154:155] op_sel_hi:[1,0]
	v_pk_mul_f32 v[162:163], v[146:147], v[154:155] op_sel_hi:[1,0]
	v_pk_fma_f32 v[88:89], v[88:89], v[160:161], v[136:137]
	v_pk_fma_f32 v[90:91], v[90:91], v[162:163], v[138:139]
	v_pk_mul_f32 v[160:161], v[148:149], v[154:155] op_sel_hi:[1,0]
	v_pk_mul_f32 v[162:163], v[150:151], v[154:155] op_sel_hi:[1,0]
	v_min_f32_e32 v88, 0x41898193, v88
	v_min_f32_e32 v89, 0x41898193, v89
	v_min_f32_e32 v90, 0x41898193, v90
	v_min_f32_e32 v91, 0x41898193, v91
	v_pk_fma_f32 v[92:93], v[92:93], v[160:161], v[140:141]
	v_pk_fma_f32 v[94:95], v[94:95], v[162:163], v[142:143]
	v_exp_f32_e64 v160, -v88
	v_exp_f32_e64 v161, -v89
	v_exp_f32_e64 v162, -v90
	v_exp_f32_e64 v163, -v91
	v_med3_f32 v92, v92, s8, v199
	v_med3_f32 v93, v93, s8, v199
	v_med3_f32 v94, v94, s8, v199
	v_med3_f32 v95, v95, s8, v199
	v_pk_add_f32 v[160:161], v[160:161], 1.0 op_sel_hi:[1,0]
	v_pk_add_f32 v[162:163], v[162:163], 1.0 op_sel_hi:[1,0]
	v_pk_fma_f32 v[92:93], v[92:93], s[100:101], s[100:101]
; #define GAS __attribute__((address_space(1)))
;     __device__ __forceinline__ void operator()(const i32x4 (&acc)[2][2][4][2], const Unit& u, int wr, int wc, int fr, int fq, PG8_LAS unsigned* scr) const {
;     ...
;             for (int mp = 0; mp < 4; mp += 2) { unsigned wp[2][2];
; #pragma unroll
;                 for (int hm = 0; hm < 2; ++hm) { const int m = mp + hm; const int r = ai * HALF + wr * 64 + m * 16 + fr; const float rs = __uint_as_float(scr[r]); float o[8];
; #pragma unroll
;                     for (int n = 0; n < 2; ++n) { const f32x4 sgr = csg[n] * rs, sur = csu[n] * rs;
; #pragma unroll
;                         for (int q = 0; q < 4; ++q) { const float h = fminf(__builtin_fmaf((float)acc[ai][0][m][n][q], sgr[q], bgv[n][q]), 7.0f * C2), up = fminf(fmaxf(__builtin_fmaf((float)acc[ai][1][m][n][q], sur[q], buv[n][q]), -7.0f), 7.0f);
;                             const float sg = __builtin_amdgcn_rcpf(1.0f + __builtin_amdgcn_exp2f(-h)); o[4 * n + q] = __builtin_fmaf(up, ACT_SC / C2, ACT_SC / C2) * (h * sg); } }
;                     int w0 = __builtin_amdgcn_cvt_pk_fp8_f32(o[0], o[1], 0, false); w0 = __builtin_amdgcn_cvt_pk_fp8_f32(o[2], o[3], w0, true);
;                     int w1 = __builtin_amdgcn_cvt_pk_fp8_f32(o[4], o[5], 0, false); w1 = __builtin_amdgcn_cvt_pk_fp8_f32(o[6], o[7], w1, true);
;                     wp[hm][0] = (unsigned)w0; wp[hm][1] = (unsigned)w1; }
;                 { auto r0 = __builtin_amdgcn_permlane16_swap(wp[0][0], wp[1][0], false, false); wp[0][0] = r0[0]; wp[1][0] = r0[1];
;                   auto r1 = __builtin_amdgcn_permlane16_swap(wp[0][1], wp[1][1], false, false); wp[0][1] = r1[0]; wp[1][1] = r1[1]; }
;                 const int odd = fq & 1;
;                 const size_t arow = (size_t)(row0 + ai * HALF + (mp + odd) * 16);
;                 *(GAS u32x4*)(act + arow * 1024 + (c0 - 8 * odd)) = (u32x4){wp[0][0], wp[0][1], wp[1][0], wp[1][1]};
;                 __builtin_amdgcn_sched_barrier(0); }
;     }
	v_pk_fma_f32 v[94:95], v[94:95], s[100:101], s[100:101]
	v_rcp_f32_e32 v160, v160
	v_rcp_f32_e32 v161, v161
	v_rcp_f32_e32 v162, v162
	v_rcp_f32_e32 v163, v163
	v_nop
	v_pk_mul_f32 v[88:89], v[88:89], v[160:161]
	v_pk_mul_f32 v[90:91], v[90:91], v[162:163]
	v_pk_mul_f32 v[88:89], v[92:93], v[88:89]
	v_pk_mul_f32 v[90:91], v[94:95], v[90:91]
	v_cvt_pk_fp8_f32 v97, v88, v89
	v_cvt_pk_fp8_f32 v97, v90, v91 op_sel:[0,0,1]
	v_cvt_f32_i32_e32 v72, v72
	v_cvt_f32_i32_e32 v73, v73
	v_cvt_f32_i32_e32 v74, v74
	v_cvt_f32_i32_e32 v75, v75
	v_cvt_f32_i32_e32 v76, v76
	v_cvt_f32_i32_e32 v77, v77
	v_cvt_f32_i32_e32 v78, v78
	v_cvt_f32_i32_e32 v79, v79
	v_pk_mul_f32 v[202:203], v[144:145], v[154:155] op_sel:[0,1] op_sel_hi:[1,1]
	v_pk_mul_f32 v[204:205], v[146:147], v[154:155] op_sel:[0,1] op_sel_hi:[1,1]
	v_pk_fma_f32 v[72:73], v[72:73], v[202:203], v[136:137]
	v_pk_fma_f32 v[74:75], v[74:75], v[204:205], v[138:139]
	v_pk_mul_f32 v[202:203], v[148:149], v[154:155] op_sel:[0,1] op_sel_hi:[1,1]
	v_pk_mul_f32 v[204:205], v[150:151], v[154:155] op_sel:[0,1] op_sel_hi:[1,1]
	v_min_f32_e32 v72, 0x41898193, v72
	v_min_f32_e32 v73, 0x41898193, v73
	v_min_f32_e32 v74, 0x41898193, v74
	v_min_f32_e32 v75, 0x41898193, v75
	v_pk_fma_f32 v[76:77], v[76:77], v[202:203], v[140:141]
	v_pk_fma_f32 v[78:79], v[78:79], v[204:205], v[142:143]
	v_exp_f32_e64 v202, -v72
	v_exp_f32_e64 v203, -v73
	v_exp_f32_e64 v204, -v74
	v_exp_f32_e64 v205, -v75
	v_med3_f32 v76, v76, s8, v199
	v_med3_f32 v77, v77, s8, v199
	v_med3_f32 v78, v78, s8, v199
	v_med3_f32 v79, v79, s8, v199
	v_pk_add_f32 v[202:203], v[202:203], 1.0 op_sel_hi:[1,0]
	v_pk_add_f32 v[204:205], v[204:205], 1.0 op_sel_hi:[1,0]
	v_pk_fma_f32 v[76:77], v[76:77], s[100:101], s[100:101]
	v_pk_fma_f32 v[78:79], v[78:79], s[100:101], s[100:101]
	v_rcp_f32_e32 v202, v202
	v_rcp_f32_e32 v203, v203
	v_rcp_f32_e32 v204, v204
	v_rcp_f32_e32 v205, v205
	v_nop
	v_pk_mul_f32 v[72:73], v[72:73], v[202:203]
	v_pk_mul_f32 v[74:75], v[74:75], v[204:205]
	v_pk_mul_f32 v[72:73], v[76:77], v[72:73]
	v_pk_mul_f32 v[74:75], v[78:79], v[74:75]
	v_cvt_pk_fp8_f32 v99, v72, v73
	v_cvt_pk_fp8_f32 v99, v74, v75 op_sel:[0,0,1]
	s_nop 1
	v_permlane16_swap_b32_e32 v96, v98
	v_permlane16_swap_b32_e32 v97, v99
	v_add_u32_e32 v160, 32, v185
	v_mov_b32_e32 v161, 0
	v_lshlrev_b64 v[160:161], 10, v[160:161]
	v_lshl_add_u64 v[160:161], s[60:61], 0, v[160:161]
	v_lshl_add_u64 v[160:161], v[160:161], 0, v[206:207]
	global_store_dwordx4 v[160:161], v[96:99], off
	v_cvt_f32_i32_e32 v56, v56
	v_cvt_f32_i32_e32 v57, v57
	v_cvt_f32_i32_e32 v58, v58
	v_cvt_f32_i32_e32 v59, v59
	v_cvt_f32_i32_e32 v60, v60
	v_cvt_f32_i32_e32 v61, v61
	v_cvt_f32_i32_e32 v62, v62
	v_cvt_f32_i32_e32 v63, v63
	v_pk_mul_f32 v[160:161], v[144:145], v[156:157] op_sel_hi:[1,0]
	v_pk_mul_f32 v[162:163], v[146:147], v[156:157] op_sel_hi:[1,0]
	v_pk_fma_f32 v[56:57], v[56:57], v[160:161], v[136:137]
	v_pk_fma_f32 v[58:59], v[58:59], v[162:163], v[138:139]
	v_pk_mul_f32 v[160:161], v[148:149], v[156:157] op_sel_hi:[1,0]
	v_pk_mul_f32 v[162:163], v[150:151], v[156:157] op_sel_hi:[1,0]
	v_min_f32_e32 v56, 0x41898193, v56
	v_min_f32_e32 v57, 0x41898193, v57
	v_min_f32_e32 v58, 0x41898193, v58
	v_min_f32_e32 v59, 0x41898193, v59
	v_pk_fma_f32 v[60:61], v[60:61], v[160:161], v[140:141]
	v_pk_fma_f32 v[62:63], v[62:63], v[162:163], v[142:143]
	v_exp_f32_e64 v160, -v56
	v_exp_f32_e64 v161, -v57
	v_exp_f32_e64 v162, -v58
	v_exp_f32_e64 v163, -v59
	v_med3_f32 v60, v60, s8, v199
	v_med3_f32 v61, v61, s8, v199
	v_med3_f32 v62, v62, s8, v199
	v_med3_f32 v63, v63, s8, v199
	v_pk_add_f32 v[160:161], v[160:161], 1.0 op_sel_hi:[1,0]
	v_pk_add_f32 v[162:163], v[162:163], 1.0 op_sel_hi:[1,0]
	v_pk_fma_f32 v[60:61], v[60:61], s[100:101], s[100:101]
	v_pk_fma_f32 v[62:63], v[62:63], s[100:101], s[100:101]
	v_rcp_f32_e32 v160, v160
	v_rcp_f32_e32 v161, v161
	v_rcp_f32_e32 v162, v162
	v_rcp_f32_e32 v163, v163
	v_nop
	v_pk_mul_f32 v[56:57], v[56:57], v[160:161]
	v_pk_mul_f32 v[58:59], v[58:59], v[162:163]
	v_pk_mul_f32 v[56:57], v[60:61], v[56:57]
	v_pk_mul_f32 v[58:59], v[62:63], v[58:59]
	v_cvt_pk_fp8_f32 v65, v56, v57
	v_cvt_pk_fp8_f32 v65, v58, v59 op_sel:[0,0,1]
	v_cvt_f32_i32_e32 v32, v32
	v_cvt_f32_i32_e32 v33, v33
	v_cvt_f32_i32_e32 v34, v34
	v_cvt_f32_i32_e32 v35, v35
	v_cvt_f32_i32_e32 v36, v36
	v_cvt_f32_i32_e32 v37, v37
	v_cvt_f32_i32_e32 v38, v38
	v_cvt_f32_i32_e32 v39, v39
	v_pk_mul_f32 v[202:203], v[144:145], v[156:157] op_sel:[0,1] op_sel_hi:[1,1]
	v_pk_mul_f32 v[204:205], v[146:147], v[156:157] op_sel:[0,1] op_sel_hi:[1,1]
	v_pk_fma_f32 v[32:33], v[32:33], v[202:203], v[136:137]
	v_pk_fma_f32 v[34:35], v[34:35], v[204:205], v[138:139]
	v_pk_mul_f32 v[202:203], v[148:149], v[156:157] op_sel:[0,1] op_sel_hi:[1,1]
	v_pk_mul_f32 v[204:205], v[150:151], v[156:157] op_sel:[0,1] op_sel_hi:[1,1]
	v_min_f32_e32 v32, 0x41898193, v32
	v_min_f32_e32 v33, 0x41898193, v33
	v_min_f32_e32 v34, 0x41898193, v34
	v_min_f32_e32 v35, 0x41898193, v35
	v_pk_fma_f32 v[36:37], v[36:37], v[202:203], v[140:141]
;     __device__ __forceinline__ void operator()(const i32x4 (&acc)[2][2][4][2], const Unit& u, int wr, int wc, int fr, int fq, PG8_LAS unsigned* scr) const {
;     ...
;             for (int mp = 0; mp < 4; mp += 2) { unsigned wp[2][2];
; #pragma unroll
;                 for (int hm = 0; hm < 2; ++hm) { const int m = mp + hm; const int r = ai * HALF + wr * 64 + m * 16 + fr; const float rs = __uint_as_float(scr[r]); float o[8];
; #pragma unroll
;                     for (int n = 0; n < 2; ++n) { const f32x4 sgr = csg[n] * rs, sur = csu[n] * rs;
; #pragma unroll
;                         for (int q = 0; q < 4; ++q) { const float h = fminf(__builtin_fmaf((float)acc[ai][0][m][n][q], sgr[q], bgv[n][q]), 7.0f * C2), up = fminf(fmaxf(__builtin_fmaf((float)acc[ai][1][m][n][q], sur[q], buv[n][q]), -7.0f), 7.0f);
;                             const float sg = __builtin_amdgcn_rcpf(1.0f + __builtin_amdgcn_exp2f(-h)); o[4 * n + q] = __builtin_fmaf(up, ACT_SC / C2, ACT_SC / C2) * (h * sg); } }
;                     int w0 = __builtin_amdgcn_cvt_pk_fp8_f32(o[0], o[1], 0, false); w0 = __builtin_amdgcn_cvt_pk_fp8_f32(o[2], o[3], w0, true);
;                     int w1 = __builtin_amdgcn_cvt_pk_fp8_f32(o[4], o[5], 0, false); w1 = __builtin_amdgcn_cvt_pk_fp8_f32(o[6], o[7], w1, true);
;                     wp[hm][0] = (unsigned)w0; wp[hm][1] = (unsigned)w1; }
;                 { auto r0 = __builtin_amdgcn_permlane16_swap(wp[0][0], wp[1][0], false, false); wp[0][0] = r0[0]; wp[1][0] = r0[1];
;                   auto r1 = __builtin_amdgcn_permlane16_swap(wp[0][1], wp[1][1], false, false); wp[0][1] = r1[0]; wp[1][1] = r1[1]; }
;                 const int odd = fq & 1;
;                 const size_t arow = (size_t)(row0 + ai * HALF + (mp + odd) * 16);
;                 *(GAS u32x4*)(act + arow * 1024 + (c0 - 8 * odd)) = (u32x4){wp[0][0], wp[0][1], wp[1][0], wp[1][1]};
;                 __builtin_amdgcn_sched_barrier(0); }
;     }
; template <class Epi, class Sched, bool GATHER, int MODE>
; __device__ __forceinline__ void gemm_phase(PG8_LAS unsigned char* lds, PG8_LAS unsigned* scr, const Gemm g, const Sched& S, const Epi& E, int tid_in) {
;     ...
;         if (!has_next) break;
;         cur = nxt; cA = nA; cB = nB; ++ui;
;         if (GATHER) { const u32x4 nx = gather_read(cur); c0[0] = nx[0]; c0[1] = nx[1]; c1[0] = nx[2]; c1[1] = nx[3]; }
;         if (wr == 1) PG8_BAR;
	v_pk_fma_f32 v[38:39], v[38:39], v[204:205], v[142:143]
	v_exp_f32_e64 v202, -v32
	v_exp_f32_e64 v203, -v33
	v_exp_f32_e64 v204, -v34
	v_exp_f32_e64 v205, -v35
	v_med3_f32 v36, v36, s8, v199
	v_med3_f32 v37, v37, s8, v199
	v_med3_f32 v38, v38, s8, v199
	v_med3_f32 v39, v39, s8, v199
	v_pk_add_f32 v[202:203], v[202:203], 1.0 op_sel_hi:[1,0]
	v_pk_add_f32 v[204:205], v[204:205], 1.0 op_sel_hi:[1,0]
	v_pk_fma_f32 v[36:37], v[36:37], s[100:101], s[100:101]
	v_pk_fma_f32 v[38:39], v[38:39], s[100:101], s[100:101]
	v_rcp_f32_e32 v202, v202
	v_rcp_f32_e32 v203, v203
	v_rcp_f32_e32 v204, v204
	v_rcp_f32_e32 v205, v205
	v_nop
	v_pk_mul_f32 v[32:33], v[32:33], v[202:203]
	v_pk_mul_f32 v[34:35], v[34:35], v[204:205]
	v_pk_mul_f32 v[32:33], v[36:37], v[32:33]
	v_pk_mul_f32 v[34:35], v[38:39], v[34:35]
	v_cvt_pk_fp8_f32 v67, v32, v33
	v_cvt_pk_fp8_f32 v67, v34, v35 op_sel:[0,0,1]
	s_nop 1
	v_permlane16_swap_b32_e32 v64, v66
	v_permlane16_swap_b32_e32 v65, v67
	v_add_u32_e32 v160, 128, v185
	v_mov_b32_e32 v161, 0
	v_lshlrev_b64 v[160:161], 10, v[160:161]
	v_lshl_add_u64 v[160:161], s[60:61], 0, v[160:161]
	v_lshl_add_u64 v[160:161], v[160:161], 0, v[206:207]
	global_store_dwordx4 v[160:161], v[64:67], off
	v_cvt_f32_i32_e32 v16, v16
	v_cvt_f32_i32_e32 v17, v17
	v_cvt_f32_i32_e32 v18, v18
	v_cvt_f32_i32_e32 v19, v19
	v_cvt_f32_i32_e32 v20, v20
	v_cvt_f32_i32_e32 v21, v21
	v_cvt_f32_i32_e32 v22, v22
	v_cvt_f32_i32_e32 v23, v23
	v_pk_mul_f32 v[160:161], v[144:145], v[158:159] op_sel_hi:[1,0]
	v_pk_mul_f32 v[162:163], v[146:147], v[158:159] op_sel_hi:[1,0]
	v_pk_fma_f32 v[16:17], v[16:17], v[160:161], v[136:137]
	v_pk_fma_f32 v[18:19], v[18:19], v[162:163], v[138:139]
	v_pk_mul_f32 v[160:161], v[148:149], v[158:159] op_sel_hi:[1,0]
	v_pk_mul_f32 v[162:163], v[150:151], v[158:159] op_sel_hi:[1,0]
	v_min_f32_e32 v16, 0x41898193, v16
	v_min_f32_e32 v17, 0x41898193, v17
	v_min_f32_e32 v18, 0x41898193, v18
	v_min_f32_e32 v19, 0x41898193, v19
	v_pk_fma_f32 v[20:21], v[20:21], v[160:161], v[140:141]
	v_pk_fma_f32 v[22:23], v[22:23], v[162:163], v[142:143]
	v_exp_f32_e64 v160, -v16
	v_exp_f32_e64 v161, -v17
	v_exp_f32_e64 v162, -v18
	v_exp_f32_e64 v163, -v19
	v_med3_f32 v20, v20, s8, v199
	v_med3_f32 v21, v21, s8, v199
	v_med3_f32 v22, v22, s8, v199
	v_med3_f32 v23, v23, s8, v199
	v_pk_add_f32 v[160:161], v[160:161], 1.0 op_sel_hi:[1,0]
	v_pk_add_f32 v[162:163], v[162:163], 1.0 op_sel_hi:[1,0]
	v_pk_fma_f32 v[20:21], v[20:21], s[100:101], s[100:101]
	v_pk_fma_f32 v[22:23], v[22:23], s[100:101], s[100:101]
	v_rcp_f32_e32 v160, v160
	v_rcp_f32_e32 v161, v161
	v_rcp_f32_e32 v162, v162
	v_rcp_f32_e32 v163, v163
	v_nop
	v_pk_mul_f32 v[16:17], v[16:17], v[160:161]
	v_pk_mul_f32 v[18:19], v[18:19], v[162:163]
	v_pk_mul_f32 v[16:17], v[20:21], v[16:17]
	v_pk_mul_f32 v[18:19], v[22:23], v[18:19]
	v_cvt_pk_fp8_f32 v25, v16, v17
	v_cvt_pk_fp8_f32 v25, v18, v19 op_sel:[0,0,1]
	v_cvt_f32_i32_e32 v0, v0
	v_cvt_f32_i32_e32 v1, v1
	v_cvt_f32_i32_e32 v2, v2
	v_cvt_f32_i32_e32 v3, v3
	v_cvt_f32_i32_e32 v4, v4
	v_cvt_f32_i32_e32 v5, v5
	v_cvt_f32_i32_e32 v6, v6
	v_cvt_f32_i32_e32 v7, v7
	v_pk_mul_f32 v[202:203], v[144:145], v[158:159] op_sel:[0,1] op_sel_hi:[1,1]
	v_pk_mul_f32 v[204:205], v[146:147], v[158:159] op_sel:[0,1] op_sel_hi:[1,1]
	v_pk_fma_f32 v[0:1], v[0:1], v[202:203], v[136:137]
	v_pk_fma_f32 v[2:3], v[2:3], v[204:205], v[138:139]
	v_pk_mul_f32 v[202:203], v[148:149], v[158:159] op_sel:[0,1] op_sel_hi:[1,1]
	v_pk_mul_f32 v[204:205], v[150:151], v[158:159] op_sel:[0,1] op_sel_hi:[1,1]
	v_min_f32_e32 v0, 0x41898193, v0
	v_min_f32_e32 v1, 0x41898193, v1
	v_min_f32_e32 v2, 0x41898193, v2
	v_min_f32_e32 v3, 0x41898193, v3
	v_pk_fma_f32 v[4:5], v[4:5], v[202:203], v[140:141]
	v_pk_fma_f32 v[6:7], v[6:7], v[204:205], v[142:143]
	v_exp_f32_e64 v202, -v0
	v_exp_f32_e64 v203, -v1
	v_exp_f32_e64 v204, -v2
	v_exp_f32_e64 v205, -v3
	v_med3_f32 v4, v4, s8, v199
	v_med3_f32 v5, v5, s8, v199
	v_med3_f32 v6, v6, s8, v199
	v_med3_f32 v7, v7, s8, v199
	v_pk_add_f32 v[202:203], v[202:203], 1.0 op_sel_hi:[1,0]
	v_pk_add_f32 v[204:205], v[204:205], 1.0 op_sel_hi:[1,0]
	v_pk_fma_f32 v[4:5], v[4:5], s[100:101], s[100:101]
	v_pk_fma_f32 v[6:7], v[6:7], s[100:101], s[100:101]
	v_rcp_f32_e32 v202, v202
	v_rcp_f32_e32 v203, v203
	v_rcp_f32_e32 v204, v204
	v_rcp_f32_e32 v205, v205
	v_nop
	v_pk_mul_f32 v[0:1], v[0:1], v[202:203]
	v_pk_mul_f32 v[2:3], v[2:3], v[204:205]
	v_pk_mul_f32 v[0:1], v[4:5], v[0:1]
	v_pk_mul_f32 v[2:3], v[6:7], v[2:3]
	v_cvt_pk_fp8_f32 v27, v0, v1
	v_cvt_pk_fp8_f32 v27, v2, v3 op_sel:[0,0,1]
	s_nop 1
	v_permlane16_swap_b32_e32 v24, v26
	v_permlane16_swap_b32_e32 v25, v27
	v_add_u32_e32 v160, 160, v185
	v_mov_b32_e32 v161, 0
	v_lshlrev_b64 v[160:161], 10, v[160:161]
	v_lshl_add_u64 v[160:161], s[60:61], 0, v[160:161]
	v_lshl_add_u64 v[160:161], v[160:161], 0, v[206:207]
	global_store_dwordx4 v[160:161], v[24:27], off
	s_cmp_eq_u32 s38, s89
	s_mov_b64 s[10:11], -1
	s_cbranch_scc1 .LBB0_786
	s_andn2_b64 vcc, exec, s[58:59]
	s_cbranch_vccnz .LBB0_785
	s_barrier
	s_branch .LBB0_785

; #define PG8_LAS __attribute__((address_space(3)))
;     __device__ __forceinline__ void operator()(const f32x4 (&acc)[2][2][4][2], const Unit& u, int wr, int wc, int fr, int fq, PG8_LAS unsigned* scr) const {
;         const int jn = u.pn & 3;
;         const int c0 = jn * 256 + wc * 32 + 8 * fq, cl = wc * 32 + 8 * fq;
;         f32x4 bv[2][2], cs[2][2];
; #pragma unroll
;         for (int bj = 0; bj < 2; ++bj)
; #pragma unroll
;             for (int n = 0; n < 2; ++n) { bv[bj][n] = *(const PG8_LAS f32x4*)(scr + 256 + bj * HALF + cl + 4 * n); cs[bj][n] = *(const PG8_LAS f32x4*)(scr + 768 + bj * HALF + cl + 4 * n) * (1.0f / (WDN_SC * ACT_SC)); }
; #pragma unroll
;         for (int ai = 0; ai < 2; ++ai)
; #pragma unroll
;             for (int mp = 0; mp < 4; mp += 2) { unsigned wq[2][2][2]; int dsts[2];
; #pragma unroll
;                 for (int hm = 0; hm < 2; ++hm) { const int m = mp + hm; const int r = ai * HALF + wr * 64 + m * 16 + fr; const int pos = u.rb * 256 + r;
;                     dsts[hm] = pos < u.cnt ? (int)scr[r] : trash + r; const float rg = __uint_as_float(scr[512 + r]) * 16.0f;
; #pragma unroll
;                     for (int bj = 0; bj < 2; ++bj) { f32x4 v0 = (acc[ai][bj][m][0] * cs[bj][0] + bv[bj][0]) * rg, v1 = (acc[ai][bj][m][1] * cs[bj][1] + bv[bj][1]) * rg;
; #pragma unroll
;                         for (int q = 0; q < 4; ++q) { v0[q] = fminf(fmaxf(v0[q], -448.0f), 448.0f); v1[q] = fminf(fmaxf(v1[q], -448.0f), 448.0f); }
;                         int w0 = __builtin_amdgcn_cvt_pk_fp8_f32(v0[0], v0[1], 0, false); w0 = __builtin_amdgcn_cvt_pk_fp8_f32(v0[2], v0[3], w0, true);
;                         int w1 = __builtin_amdgcn_cvt_pk_fp8_f32(v1[0], v1[1], 0, false); w1 = __builtin_amdgcn_cvt_pk_fp8_f32(v1[2], v1[3], w1, true);
;                         wq[hm][bj][0] = (unsigned)w0; wq[hm][bj][1] = (unsigned)w1; } }
.LBB0_961:
	v_mov_b32_e32 v168, v182
	s_movk_i32 s36, 0xffc0
	v_lshlrev_b32_e32 v0, 1, v168
	v_and_b32_e32 v0, 0x1e0, v0
	v_add_u32_e32 v0, 0, v0
	v_add_u32_e32 v1, 0x20d00, v0
	v_add_u32_e32 v16, 0x21500, v0
	ds_read_b128 v[12:15], v1
	ds_read_b128 v[8:11], v1 offset:16
	ds_read_b128 v[28:31], v16
	ds_read_b128 v[20:23], v16 offset:16
	ds_read_b128 v[4:7], v1 offset:512
	ds_read_b128 v[0:3], v1 offset:528
	ds_read_b128 v[24:27], v16 offset:512
	ds_read_b128 v[16:19], v16 offset:528
	v_and_b32_e32 v32, 15, v168
	v_ashrrev_i32_e32 v33, 2, v168
	v_and_or_b32 v37, v33, s36, v32
	s_lshl_b32 s42, s76, 8
	v_add_u32_e32 v38, s42, v37
	v_cmp_le_i32_e32 vcc, s69, v38
	s_and_saveexec_b64 s[36:37], vcc
	s_xor_b64 s[36:37], exec, s[36:37]
	v_add_u32_e32 v39, 0x40000, v37
	s_andn2_saveexec_b64 s[36:37], s[36:37]
	v_lshl_add_u32 v32, v37, 2, 0
	v_add_u32_e32 v32, 0x20900, v32
	ds_read_b32 v39, v32
	s_or_b64 exec, exec, s[36:37]
	v_lshl_add_u32 v36, v37, 2, s88
	ds_read_b32 v209, v36 offset:2048
	v_or_b32_e32 v208, 16, v37
	v_add_u32_e32 v32, s42, v208
	v_cmp_le_i32_e32 vcc, s69, v32
	s_and_saveexec_b64 s[36:37], vcc
	s_xor_b64 s[36:37], exec, s[36:37]
	v_add_u32_e32 v207, 0x40010, v37
	s_andn2_saveexec_b64 s[36:37], s[36:37]
	v_lshl_add_u32 v32, v208, 2, 0
	v_add_u32_e32 v32, 0x20900, v32
	ds_read_b32 v207, v32
	s_or_b64 exec, exec, s[36:37]
	s_and_b64 s[98:99], exec, s[44:45]
	s_cbranch_scc0 .Lp6_epi_nobar
	s_barrier
.Lp6_epi_nobar:
	s_mov_b32 s36, 0x39929cec
	s_waitcnt lgkmcnt(6)
	v_pk_mul_f32 v[32:33], v[30:31], s[36:37] op_sel_hi:[1,0]
	v_pk_mul_f32 v[34:35], v[28:29], s[36:37] op_sel_hi:[1,0]
	s_waitcnt lgkmcnt(5)
	v_pk_mul_f32 v[28:29], v[22:23], s[36:37] op_sel_hi:[1,0]
	v_pk_mul_f32 v[30:31], v[20:21], s[36:37] op_sel_hi:[1,0]
	s_waitcnt lgkmcnt(2)
	v_pk_mul_f32 v[20:21], v[26:27], s[36:37] op_sel_hi:[1,0]
	v_pk_mul_f32 v[22:23], v[24:25], s[36:37] op_sel_hi:[1,0]
	s_waitcnt lgkmcnt(0)
	v_mul_f32_e32 v26, 0x41800000, v209
	v_pk_fma_f32 v[24:25], v[154:155], v[32:33], v[14:15]
	v_pk_fma_f32 v[152:153], v[152:153], v[34:35], v[12:13]
	v_pk_mul_f32 v[154:155], v[24:25], v[26:27] op_sel_hi:[1,0]
	v_pk_mul_f32 v[24:25], v[152:153], v[26:27] op_sel_hi:[1,0]
	v_pk_fma_f32 v[152:153], v[158:159], v[28:29], v[10:11]
	v_pk_fma_f32 v[156:157], v[156:157], v[30:31], v[8:9]
	v_pk_mul_f32 v[152:153], v[152:153], v[26:27] op_sel_hi:[1,0]
	v_pk_mul_f32 v[156:157], v[156:157], v[26:27] op_sel_hi:[1,0]
	v_med3_f32 v27, v24, s9, v200
	v_med3_f32 v25, v25, s9, v200
	v_mov_b32_e32 v24, v169
	v_med3_f32 v156, v156, s9, v200
	v_med3_f32 v157, v157, s9, v200
	v_cvt_pk_fp8_f32 v24, v27, v25
	v_mov_b32_e32 v25, v169
	v_cvt_pk_fp8_f32 v25, v156, v157
	v_med3_f32 v154, v154, s9, v200
	v_med3_f32 v152, v152, s9, v200
	v_med3_f32 v27, v155, s9, v200
	v_med3_f32 v153, v153, s9, v200
	v_pk_mul_f32 v[18:19], v[18:19], s[36:37] op_sel_hi:[1,0]
	v_pk_mul_f32 v[16:17], v[16:17], s[36:37] op_sel_hi:[1,0]
	v_cvt_pk_fp8_f32 v24, v154, v27 op_sel:[0,0,1]
	v_cvt_pk_fp8_f32 v25, v152, v153 op_sel:[0,0,1]
	v_pk_fma_f32 v[152:153], v[162:163], v[20:21], v[6:7]
	v_pk_fma_f32 v[154:155], v[160:161], v[22:23], v[4:5]
	v_pk_mul_f32 v[156:157], v[152:153], v[26:27] op_sel_hi:[1,0]
	v_pk_mul_f32 v[152:153], v[154:155], v[26:27] op_sel_hi:[1,0]
	v_pk_fma_f32 v[154:155], v[166:167], v[18:19], v[2:3]
	v_pk_fma_f32 v[158:159], v[164:165], v[16:17], v[0:1]
	v_pk_mul_f32 v[154:155], v[154:155], v[26:27] op_sel_hi:[1,0]
	v_pk_mul_f32 v[26:27], v[158:159], v[26:27] op_sel_hi:[1,0]
	v_med3_f32 v158, v152, s9, v200
	v_med3_f32 v153, v153, s9, v200
	v_mov_b32_e32 v152, v169
	v_cvt_pk_fp8_f32 v152, v158, v153
	v_med3_f32 v26, v26, s9, v200
	v_med3_f32 v27, v27, s9, v200
	v_mov_b32_e32 v153, v169
	v_med3_f32 v156, v156, s9, v200
	v_cvt_pk_fp8_f32 v153, v26, v27
	v_med3_f32 v26, v157, s9, v200
	v_cvt_pk_fp8_f32 v152, v156, v26 op_sel:[0,0,1]
	v_lshl_add_u32 v26, v208, 2, s88
	ds_read_b32 v26, v26 offset:2048
	v_lshrrev_b32_e32 v210, 1, v168
	v_med3_f32 v154, v154, s9, v200
	v_med3_f32 v27, v155, s9, v200
	s_lshl_b32 s36, s75, 8
	v_cvt_pk_fp8_f32 v153, v154, v27 op_sel:[0,0,1]
	s_and_b32 s36, s36, 0x300
	v_and_b32_e32 v27, 0x70, v210
	v_and_b32_e32 v156, 16, v168
	v_or_b32_e32 v168, s36, v27
	s_waitcnt lgkmcnt(0)
	v_mul_f32_e32 v154, 0x41800000, v26
	v_pk_fma_f32 v[26:27], v[142:143], v[32:33], v[14:15]
	v_pk_fma_f32 v[140:141], v[140:141], v[34:35], v[12:13]
	v_pk_mul_f32 v[142:143], v[26:27], v[154:155] op_sel_hi:[1,0]
	v_pk_mul_f32 v[26:27], v[140:141], v[154:155] op_sel_hi:[1,0]
	v_pk_fma_f32 v[136:137], v[136:137], v[30:31], v[8:9]
	v_med3_f32 v140, v26, s9, v200
	v_pk_mul_f32 v[136:137], v[136:137], v[154:155] op_sel_hi:[1,0]
	v_med3_f32 v27, v27, s9, v200
	v_mov_b32_e32 v26, v169
	v_med3_f32 v136, v136, s9, v200
	v_med3_f32 v137, v137, s9, v200
	v_cvt_pk_fp8_f32 v26, v140, v27
	v_mov_b32_e32 v27, v169
	v_cvt_pk_fp8_f32 v27, v136, v137
	v_pk_fma_f32 v[138:139], v[138:139], v[28:29], v[10:11]
	v_med3_f32 v141, v142, s9, v200
	v_pk_mul_f32 v[138:139], v[138:139], v[154:155] op_sel_hi:[1,0]
	v_med3_f32 v136, v143, s9, v200
	v_med3_f32 v138, v138, s9, v200
	v_med3_f32 v137, v139, s9, v200
	v_cvt_pk_fp8_f32 v27, v138, v137 op_sel:[0,0,1]
	v_pk_fma_f32 v[138:139], v[148:149], v[22:23], v[4:5]
	v_cvt_pk_fp8_f32 v26, v141, v136 op_sel:[0,0,1]
	v_pk_fma_f32 v[136:137], v[150:151], v[20:21], v[6:7]
	v_pk_mul_f32 v[138:139], v[138:139], v[154:155] op_sel_hi:[1,0]
	v_pk_fma_f32 v[140:141], v[146:147], v[18:19], v[2:3]
	v_pk_fma_f32 v[142:143], v[144:145], v[16:17], v[0:1]
	v_pk_mul_f32 v[136:137], v[136:137], v[154:155] op_sel_hi:[1,0]
	v_pk_mul_f32 v[140:141], v[140:141], v[154:155] op_sel_hi:[1,0]
; #define GAS __attribute__((address_space(1)))
;     __device__ __forceinline__ void operator()(const f32x4 (&acc)[2][2][4][2], const Unit& u, int wr, int wc, int fr, int fq, PG8_LAS unsigned* scr) const {
;     ...
;                 for (int hm = 0; hm < 2; ++hm) { const int m = mp + hm; const int r = ai * HALF + wr * 64 + m * 16 + fr; const int pos = u.rb * 256 + r;
;                     dsts[hm] = pos < u.cnt ? (int)scr[r] : trash + r; const float rg = __uint_as_float(scr[512 + r]) * 16.0f;
; #pragma unroll
;                     for (int bj = 0; bj < 2; ++bj) { f32x4 v0 = (acc[ai][bj][m][0] * cs[bj][0] + bv[bj][0]) * rg, v1 = (acc[ai][bj][m][1] * cs[bj][1] + bv[bj][1]) * rg;
; #pragma unroll
;                         for (int q = 0; q < 4; ++q) { v0[q] = fminf(fmaxf(v0[q], -448.0f), 448.0f); v1[q] = fminf(fmaxf(v1[q], -448.0f), 448.0f); }
;                         int w0 = __builtin_amdgcn_cvt_pk_fp8_f32(v0[0], v0[1], 0, false); w0 = __builtin_amdgcn_cvt_pk_fp8_f32(v0[2], v0[3], w0, true);
;                         int w1 = __builtin_amdgcn_cvt_pk_fp8_f32(v1[0], v1[1], 0, false); w1 = __builtin_amdgcn_cvt_pk_fp8_f32(v1[2], v1[3], w1, true);
;                         wq[hm][bj][0] = (unsigned)w0; wq[hm][bj][1] = (unsigned)w1; } }
;                 const int odd = fq & 1; unsigned char* rowp = (unsigned char*)y4 + (size_t)(odd ? dsts[1] : dsts[0]) * 1024 + (c0 - 8 * odd);
; #pragma unroll
;                 for (int bj = 0; bj < 2; ++bj) {
;                     auto r0 = __builtin_amdgcn_permlane16_swap(wq[0][bj][0], wq[1][bj][0], false, false); auto r1 = __builtin_amdgcn_permlane16_swap(wq[0][bj][1], wq[1][bj][1], false, false);
;                     *(GAS u32x4*)(rowp + bj * HALF) = (u32x4){(unsigned)r0[0], (unsigned)r1[0], (unsigned)r0[1], (unsigned)r1[1]}; } }
	v_pk_mul_f32 v[142:143], v[142:143], v[154:155] op_sel_hi:[1,0]
	v_med3_f32 v138, v138, s9, v200
	v_med3_f32 v139, v139, s9, v200
	v_mov_b32_e32 v154, v169
	v_cvt_pk_fp8_f32 v154, v138, v139
	v_med3_f32 v142, v142, s9, v200
	v_med3_f32 v143, v143, s9, v200
	v_mov_b32_e32 v155, v169
	v_med3_f32 v136, v136, s9, v200
	v_cvt_pk_fp8_f32 v155, v142, v143
	v_med3_f32 v137, v137, s9, v200
	v_cmp_eq_u32_e32 vcc, 0, v156
	v_cvt_pk_fp8_f32 v154, v136, v137 op_sel:[0,0,1]
	v_med3_f32 v140, v140, s9, v200
	v_cndmask_b32_e32 v136, v207, v39, vcc
	v_ashrrev_i32_e32 v137, 31, v136
	v_med3_f32 v138, v141, s9, v200
	v_lshlrev_b64 v[136:137], 10, v[136:137]
	v_cvt_pk_fp8_f32 v155, v140, v138 op_sel:[0,0,1]
	v_lshl_add_u64 v[136:137], s[30:31], 0, v[136:137]
	v_lshl_add_u64 v[136:137], v[136:137], 0, v[168:169]
	v_permlane16_swap_b32_e32 v24, v26
	v_permlane16_swap_b32_e32 v25, v27
	global_store_dwordx4 v[136:137], v[24:27], off
	v_permlane16_swap_b32_e32 v152, v154
	s_nop 0
	v_or_b32_e32 v25, 32, v37
	v_add_u32_e32 v24, s42, v25
	v_permlane16_swap_b32_e32 v153, v155
	v_cmp_le_i32_e64 s[36:37], s69, v24
	global_store_dwordx4 v[136:137], v[152:155], off offset:128
	s_and_saveexec_b64 s[76:77], s[36:37]
	s_xor_b64 s[36:37], exec, s[76:77]
	v_add_u32_e32 v24, 0x40020, v37
	s_andn2_saveexec_b64 s[36:37], s[36:37]
	v_lshl_add_u32 v24, v25, 2, 0
	v_add_u32_e32 v24, 0x20900, v24
	ds_read_b32 v24, v24
	s_or_b64 exec, exec, s[36:37]
	v_lshl_add_u32 v25, v25, 2, s88
	ds_read_b32 v27, v25 offset:2048
	v_or_b32_e32 v26, 48, v37
	v_add_u32_e32 v25, s42, v26
	v_cmp_le_i32_e64 s[36:37], s69, v25
	s_and_saveexec_b64 s[42:43], s[36:37]
	s_xor_b64 s[36:37], exec, s[42:43]
	v_add_u32_e32 v25, 0x40030, v37
	s_andn2_saveexec_b64 s[36:37], s[36:37]
	v_lshl_add_u32 v25, v26, 2, 0
	v_add_u32_e32 v25, 0x20900, v25
	ds_read_b32 v25, v25
	s_or_b64 exec, exec, s[36:37]
	s_waitcnt lgkmcnt(0)
	v_mul_f32_e32 v136, 0x41800000, v27
	v_pk_fma_f32 v[132:133], v[132:133], v[34:35], v[12:13]
	v_pk_fma_f32 v[124:125], v[124:125], v[30:31], v[8:9]
	v_pk_mul_f32 v[132:133], v[132:133], v[136:137] op_sel_hi:[1,0]
	v_pk_mul_f32 v[124:125], v[124:125], v[136:137] op_sel_hi:[1,0]
	v_med3_f32 v27, v132, s9, v200
	v_med3_f32 v39, v124, s9, v200
	v_med3_f32 v132, v133, s9, v200
	v_med3_f32 v133, v125, s9, v200
	v_mov_b32_e32 v124, v169
	v_mov_b32_e32 v125, v169
	v_cvt_pk_fp8_f32 v124, v27, v132
	v_cvt_pk_fp8_f32 v125, v39, v133
	v_pk_fma_f32 v[134:135], v[134:135], v[32:33], v[14:15]
	v_pk_fma_f32 v[126:127], v[126:127], v[28:29], v[10:11]
	v_lshl_add_u32 v26, v26, 2, s88
	v_pk_mul_f32 v[134:135], v[134:135], v[136:137] op_sel_hi:[1,0]
	v_pk_mul_f32 v[126:127], v[126:127], v[136:137] op_sel_hi:[1,0]
	v_pk_fma_f32 v[128:129], v[128:129], v[22:23], v[4:5]
	v_pk_fma_f32 v[120:121], v[120:121], v[16:17], v[0:1]
	ds_read_b32 v26, v26 offset:2048
	v_med3_f32 v134, v134, s9, v200
	v_med3_f32 v126, v126, s9, v200
	v_med3_f32 v27, v135, s9, v200
	v_med3_f32 v39, v127, s9, v200
	v_pk_mul_f32 v[128:129], v[128:129], v[136:137] op_sel_hi:[1,0]
	v_pk_mul_f32 v[120:121], v[120:121], v[136:137] op_sel_hi:[1,0]
	v_cvt_pk_fp8_f32 v124, v134, v27 op_sel:[0,0,1]
	v_cvt_pk_fp8_f32 v125, v126, v39 op_sel:[0,0,1]
	v_med3_f32 v27, v128, s9, v200
	v_med3_f32 v39, v120, s9, v200
	v_med3_f32 v128, v129, s9, v200
	v_med3_f32 v129, v121, s9, v200
	v_mov_b32_e32 v121, v169
	v_pk_fma_f32 v[126:127], v[130:131], v[20:21], v[6:7]
	v_mov_b32_e32 v120, v169
	v_cvt_pk_fp8_f32 v121, v39, v129
	v_pk_mul_f32 v[126:127], v[126:127], v[136:137] op_sel_hi:[1,0]
	v_pk_fma_f32 v[122:123], v[122:123], v[18:19], v[2:3]
	v_cvt_pk_fp8_f32 v120, v27, v128
	v_pk_mul_f32 v[122:123], v[122:123], v[136:137] op_sel_hi:[1,0]
	v_med3_f32 v27, v127, s9, v200
	s_waitcnt lgkmcnt(0)
	v_mul_f32_e32 v26, 0x41800000, v26
	v_pk_fma_f32 v[108:109], v[108:109], v[30:31], v[8:9]
	v_med3_f32 v122, v122, s9, v200
	v_med3_f32 v39, v123, s9, v200
	v_pk_fma_f32 v[116:117], v[116:117], v[34:35], v[12:13]
	v_pk_mul_f32 v[108:109], v[108:109], v[26:27] op_sel_hi:[1,0]
	v_med3_f32 v126, v126, s9, v200
	v_cvt_pk_fp8_f32 v121, v122, v39 op_sel:[0,0,1]
	v_pk_fma_f32 v[118:119], v[118:119], v[32:33], v[14:15]
	v_pk_mul_f32 v[116:117], v[116:117], v[26:27] op_sel_hi:[1,0]
	v_pk_fma_f32 v[110:111], v[110:111], v[28:29], v[10:11]
	v_med3_f32 v39, v108, s9, v200
	v_med3_f32 v109, v109, s9, v200
	v_mov_b32_e32 v127, v169
	v_cvt_pk_fp8_f32 v120, v126, v27 op_sel:[0,0,1]
	v_pk_mul_f32 v[118:119], v[118:119], v[26:27] op_sel_hi:[1,0]
	v_pk_mul_f32 v[110:111], v[110:111], v[26:27] op_sel_hi:[1,0]
	v_med3_f32 v27, v116, s9, v200
	v_med3_f32 v108, v117, s9, v200
	v_mov_b32_e32 v126, v169
	v_cvt_pk_fp8_f32 v127, v39, v109
	v_cvt_pk_fp8_f32 v126, v27, v108
	v_med3_f32 v110, v110, s9, v200
	v_med3_f32 v39, v111, s9, v200
	v_med3_f32 v116, v118, s9, v200
	v_med3_f32 v27, v119, s9, v200
	v_cvt_pk_fp8_f32 v127, v110, v39 op_sel:[0,0,1]
	v_pk_fma_f32 v[108:109], v[114:115], v[20:21], v[6:7]
	v_pk_fma_f32 v[110:111], v[112:113], v[22:23], v[4:5]
	v_pk_fma_f32 v[106:107], v[106:107], v[18:19], v[2:3]
	v_pk_fma_f32 v[104:105], v[104:105], v[16:17], v[0:1]
	v_cvt_pk_fp8_f32 v126, v116, v27 op_sel:[0,0,1]
	v_pk_mul_f32 v[108:109], v[108:109], v[26:27] op_sel_hi:[1,0]
	v_pk_mul_f32 v[110:111], v[110:111], v[26:27] op_sel_hi:[1,0]
	v_pk_mul_f32 v[106:107], v[106:107], v[26:27] op_sel_hi:[1,0]
	v_pk_mul_f32 v[26:27], v[104:105], v[26:27] op_sel_hi:[1,0]
	v_med3_f32 v39, v110, s9, v200
	v_med3_f32 v26, v26, s9, v200
	v_med3_f32 v104, v111, s9, v200
	v_med3_f32 v27, v27, s9, v200
	v_mov_b32_e32 v122, v169
	v_mov_b32_e32 v123, v169
	v_cvt_pk_fp8_f32 v122, v39, v104
	v_cvt_pk_fp8_f32 v123, v26, v27
	v_med3_f32 v105, v108, s9, v200
	v_med3_f32 v106, v106, s9, v200
	v_med3_f32 v26, v109, s9, v200
	v_med3_f32 v27, v107, s9, v200
	v_cvt_pk_fp8_f32 v122, v105, v26 op_sel:[0,0,1]
	v_cvt_pk_fp8_f32 v123, v106, v27 op_sel:[0,0,1]
	v_cndmask_b32_e32 v24, v25, v24, vcc
	v_ashrrev_i32_e32 v25, 31, v24
	v_lshlrev_b64 v[24:25], 10, v[24:25]
	v_lshl_add_u64 v[24:25], s[30:31], 0, v[24:25]
	v_lshl_add_u64 v[24:25], v[24:25], 0, v[168:169]
	v_permlane16_swap_b32_e32 v124, v126
	v_permlane16_swap_b32_e32 v125, v127
	v_permlane16_swap_b32_e32 v120, v122
	v_permlane16_swap_b32_e32 v121, v123
	global_store_dwordx4 v[24:25], v[124:127], off
	global_store_dwordx4 v[24:25], v[120:123], off offset:128
	v_add_u32_e32 v24, 0x80, v38
	v_cmp_le_i32_e64 s[36:37], s69, v24
	s_and_saveexec_b64 s[42:43], s[36:37]
	s_xor_b64 s[36:37], exec, s[42:43]
	v_add_u32_e32 v24, 0x40080, v37
	s_andn2_saveexec_b64 s[36:37], s[36:37]
	ds_read_b32 v24, v36 offset:512
	s_or_b64 exec, exec, s[36:37]
	ds_read_b32 v26, v36 offset:2560
	v_add_u32_e32 v25, 0x90, v38
	v_cmp_le_i32_e64 s[36:37], s69, v25
	s_and_saveexec_b64 s[42:43], s[36:37]
	s_xor_b64 s[36:37], exec, s[42:43]
	v_add_u32_e32 v25, 0x40090, v37
	s_andn2_saveexec_b64 s[36:37], s[36:37]
	ds_read_b32 v25, v36 offset:576
	s_or_b64 exec, exec, s[36:37]
	s_waitcnt lgkmcnt(0)
; #define GAS __attribute__((address_space(1)))
;     __device__ __forceinline__ void operator()(const f32x4 (&acc)[2][2][4][2], const Unit& u, int wr, int wc, int fr, int fq, PG8_LAS unsigned* scr) const {
;     ...
;                 for (int hm = 0; hm < 2; ++hm) { const int m = mp + hm; const int r = ai * HALF + wr * 64 + m * 16 + fr; const int pos = u.rb * 256 + r;
;                     dsts[hm] = pos < u.cnt ? (int)scr[r] : trash + r; const float rg = __uint_as_float(scr[512 + r]) * 16.0f;
; #pragma unroll
;                     for (int bj = 0; bj < 2; ++bj) { f32x4 v0 = (acc[ai][bj][m][0] * cs[bj][0] + bv[bj][0]) * rg, v1 = (acc[ai][bj][m][1] * cs[bj][1] + bv[bj][1]) * rg;
; #pragma unroll
;                         for (int q = 0; q < 4; ++q) { v0[q] = fminf(fmaxf(v0[q], -448.0f), 448.0f); v1[q] = fminf(fmaxf(v1[q], -448.0f), 448.0f); }
;                         int w0 = __builtin_amdgcn_cvt_pk_fp8_f32(v0[0], v0[1], 0, false); w0 = __builtin_amdgcn_cvt_pk_fp8_f32(v0[2], v0[3], w0, true);
;                         int w1 = __builtin_amdgcn_cvt_pk_fp8_f32(v1[0], v1[1], 0, false); w1 = __builtin_amdgcn_cvt_pk_fp8_f32(v1[2], v1[3], w1, true);
;                         wq[hm][bj][0] = (unsigned)w0; wq[hm][bj][1] = (unsigned)w1; } }
;                 const int odd = fq & 1; unsigned char* rowp = (unsigned char*)y4 + (size_t)(odd ? dsts[1] : dsts[0]) * 1024 + (c0 - 8 * odd);
; #pragma unroll
;                 for (int bj = 0; bj < 2; ++bj) {
;                     auto r0 = __builtin_amdgcn_permlane16_swap(wq[0][bj][0], wq[1][bj][0], false, false); auto r1 = __builtin_amdgcn_permlane16_swap(wq[0][bj][1], wq[1][bj][1], false, false);
;                     *(GAS u32x4*)(rowp + bj * HALF) = (u32x4){(unsigned)r0[0], (unsigned)r1[0], (unsigned)r0[1], (unsigned)r1[1]}; } }
	v_mul_f32_e32 v26, 0x41800000, v26
	v_pk_fma_f32 v[96:97], v[96:97], v[34:35], v[12:13]
	v_pk_fma_f32 v[88:89], v[88:89], v[30:31], v[8:9]
	v_pk_fma_f32 v[98:99], v[98:99], v[32:33], v[14:15]
	v_pk_mul_f32 v[96:97], v[96:97], v[26:27] op_sel_hi:[1,0]
	v_pk_fma_f32 v[90:91], v[90:91], v[28:29], v[10:11]
	v_pk_mul_f32 v[88:89], v[88:89], v[26:27] op_sel_hi:[1,0]
	v_pk_mul_f32 v[98:99], v[98:99], v[26:27] op_sel_hi:[1,0]
	v_pk_mul_f32 v[90:91], v[90:91], v[26:27] op_sel_hi:[1,0]
	v_med3_f32 v27, v96, s9, v200
	v_med3_f32 v39, v88, s9, v200
	v_med3_f32 v96, v97, s9, v200
	v_med3_f32 v97, v89, s9, v200
	v_mov_b32_e32 v89, v169
	v_mov_b32_e32 v88, v169
	v_cvt_pk_fp8_f32 v89, v39, v97
	v_cvt_pk_fp8_f32 v88, v27, v96
	v_med3_f32 v90, v90, s9, v200
	v_med3_f32 v27, v99, s9, v200
	v_med3_f32 v39, v91, s9, v200
	v_pk_fma_f32 v[96:97], v[100:101], v[22:23], v[4:5]
	v_med3_f32 v98, v98, s9, v200
	v_cvt_pk_fp8_f32 v89, v90, v39 op_sel:[0,0,1]
	v_pk_fma_f32 v[90:91], v[102:103], v[20:21], v[6:7]
	v_pk_mul_f32 v[96:97], v[96:97], v[26:27] op_sel_hi:[1,0]
	v_pk_fma_f32 v[94:95], v[94:95], v[18:19], v[2:3]
	v_pk_fma_f32 v[92:93], v[92:93], v[16:17], v[0:1]
	v_cvt_pk_fp8_f32 v88, v98, v27 op_sel:[0,0,1]
	v_pk_mul_f32 v[90:91], v[90:91], v[26:27] op_sel_hi:[1,0]
	v_pk_mul_f32 v[94:95], v[94:95], v[26:27] op_sel_hi:[1,0]
	v_pk_mul_f32 v[26:27], v[92:93], v[26:27] op_sel_hi:[1,0]
	v_med3_f32 v39, v96, s9, v200
	v_med3_f32 v93, v97, s9, v200
	v_mov_b32_e32 v92, v169
	v_med3_f32 v26, v26, s9, v200
	v_med3_f32 v27, v27, s9, v200
	v_cvt_pk_fp8_f32 v92, v39, v93
	v_mov_b32_e32 v93, v169
	v_cvt_pk_fp8_f32 v93, v26, v27
	ds_read_b32 v26, v36 offset:2624
	v_med3_f32 v27, v91, s9, v200
	v_pk_fma_f32 v[84:85], v[84:85], v[34:35], v[12:13]
	v_pk_fma_f32 v[80:81], v[80:81], v[30:31], v[8:9]
	v_med3_f32 v90, v90, s9, v200
	s_waitcnt lgkmcnt(0)
	v_mul_f32_e32 v26, 0x41800000, v26
	v_med3_f32 v94, v94, s9, v200
	v_med3_f32 v39, v95, s9, v200
	v_pk_fma_f32 v[86:87], v[86:87], v[32:33], v[14:15]
	v_pk_mul_f32 v[84:85], v[84:85], v[26:27] op_sel_hi:[1,0]
	v_pk_fma_f32 v[82:83], v[82:83], v[28:29], v[10:11]
	v_pk_mul_f32 v[80:81], v[80:81], v[26:27] op_sel_hi:[1,0]
	v_cvt_pk_fp8_f32 v92, v90, v27 op_sel:[0,0,1]
	v_cvt_pk_fp8_f32 v93, v94, v39 op_sel:[0,0,1]
	v_pk_mul_f32 v[86:87], v[86:87], v[26:27] op_sel_hi:[1,0]
	v_pk_mul_f32 v[82:83], v[82:83], v[26:27] op_sel_hi:[1,0]
	v_med3_f32 v27, v84, s9, v200
	v_med3_f32 v39, v80, s9, v200
	v_med3_f32 v80, v85, s9, v200
	v_mov_b32_e32 v90, v169
	v_med3_f32 v81, v81, s9, v200
	v_cvt_pk_fp8_f32 v90, v27, v80
	v_mov_b32_e32 v91, v169
	v_cvt_pk_fp8_f32 v91, v39, v81
	v_med3_f32 v84, v86, s9, v200
	v_med3_f32 v27, v87, s9, v200
	v_pk_fma_f32 v[62:63], v[62:63], v[20:21], v[6:7]
	v_pk_fma_f32 v[60:61], v[60:61], v[22:23], v[4:5]
	v_pk_fma_f32 v[58:59], v[58:59], v[18:19], v[2:3]
	v_pk_fma_f32 v[56:57], v[56:57], v[16:17], v[0:1]
	v_med3_f32 v82, v82, s9, v200
	v_med3_f32 v39, v83, s9, v200
	v_cvt_pk_fp8_f32 v90, v84, v27 op_sel:[0,0,1]
	v_pk_mul_f32 v[62:63], v[62:63], v[26:27] op_sel_hi:[1,0]
	v_pk_mul_f32 v[60:61], v[60:61], v[26:27] op_sel_hi:[1,0]
	v_pk_mul_f32 v[58:59], v[58:59], v[26:27] op_sel_hi:[1,0]
	v_pk_mul_f32 v[26:27], v[56:57], v[26:27] op_sel_hi:[1,0]
	v_cvt_pk_fp8_f32 v91, v82, v39 op_sel:[0,0,1]
	v_med3_f32 v39, v60, s9, v200
	v_med3_f32 v26, v26, s9, v200
	v_med3_f32 v56, v61, s9, v200
	v_med3_f32 v27, v27, s9, v200
	v_mov_b32_e32 v94, v169
	v_mov_b32_e32 v95, v169
	v_cvt_pk_fp8_f32 v94, v39, v56
	v_cvt_pk_fp8_f32 v95, v26, v27
	v_med3_f32 v57, v62, s9, v200
	v_med3_f32 v58, v58, s9, v200
	v_med3_f32 v26, v63, s9, v200
	v_med3_f32 v27, v59, s9, v200
	v_cvt_pk_fp8_f32 v94, v57, v26 op_sel:[0,0,1]
	v_cvt_pk_fp8_f32 v95, v58, v27 op_sel:[0,0,1]
	v_cndmask_b32_e32 v24, v25, v24, vcc
	v_ashrrev_i32_e32 v25, 31, v24
	v_lshlrev_b64 v[24:25], 10, v[24:25]
	v_lshl_add_u64 v[24:25], s[30:31], 0, v[24:25]
	v_lshl_add_u64 v[24:25], v[24:25], 0, v[168:169]
	v_permlane16_swap_b32_e32 v88, v90
	v_permlane16_swap_b32_e32 v89, v91
	v_permlane16_swap_b32_e32 v92, v94
	v_permlane16_swap_b32_e32 v93, v95
	global_store_dwordx4 v[24:25], v[88:91], off
	global_store_dwordx4 v[24:25], v[92:95], off offset:128
	v_add_u32_e32 v24, 0xa0, v38
	v_cmp_le_i32_e64 s[36:37], s69, v24
	s_and_saveexec_b64 s[42:43], s[36:37]
	s_xor_b64 s[36:37], exec, s[42:43]
	v_add_u32_e32 v24, 0x400a0, v37
	s_andn2_saveexec_b64 s[36:37], s[36:37]
	ds_read_b32 v24, v36 offset:640
	s_or_b64 exec, exec, s[36:37]
	ds_read_b32 v26, v36 offset:2688
	v_add_u32_e32 v25, 0xb0, v38
	v_cmp_le_i32_e64 s[36:37], s69, v25
	s_and_saveexec_b64 s[42:43], s[36:37]
	s_xor_b64 s[36:37], exec, s[42:43]
	v_add_u32_e32 v25, 0x400b0, v37
	s_andn2_saveexec_b64 s[36:37], s[36:37]
	ds_read_b32 v25, v36 offset:704
	s_or_b64 exec, exec, s[36:37]
	s_waitcnt lgkmcnt(0)
; #define GAS __attribute__((address_space(1)))
; #define PG8_BAR __builtin_amdgcn_s_barrier()
;     __device__ __forceinline__ void operator()(const f32x4 (&acc)[2][2][4][2], const Unit& u, int wr, int wc, int fr, int fq, PG8_LAS unsigned* scr) const {
;     ...
;                 for (int hm = 0; hm < 2; ++hm) { const int m = mp + hm; const int r = ai * HALF + wr * 64 + m * 16 + fr; const int pos = u.rb * 256 + r;
;                     dsts[hm] = pos < u.cnt ? (int)scr[r] : trash + r; const float rg = __uint_as_float(scr[512 + r]) * 16.0f;
; #pragma unroll
;                     for (int bj = 0; bj < 2; ++bj) { f32x4 v0 = (acc[ai][bj][m][0] * cs[bj][0] + bv[bj][0]) * rg, v1 = (acc[ai][bj][m][1] * cs[bj][1] + bv[bj][1]) * rg;
; #pragma unroll
;                         for (int q = 0; q < 4; ++q) { v0[q] = fminf(fmaxf(v0[q], -448.0f), 448.0f); v1[q] = fminf(fmaxf(v1[q], -448.0f), 448.0f); }
;                         int w0 = __builtin_amdgcn_cvt_pk_fp8_f32(v0[0], v0[1], 0, false); w0 = __builtin_amdgcn_cvt_pk_fp8_f32(v0[2], v0[3], w0, true);
;                         int w1 = __builtin_amdgcn_cvt_pk_fp8_f32(v1[0], v1[1], 0, false); w1 = __builtin_amdgcn_cvt_pk_fp8_f32(v1[2], v1[3], w1, true);
;                         wq[hm][bj][0] = (unsigned)w0; wq[hm][bj][1] = (unsigned)w1; } }
;                 const int odd = fq & 1; unsigned char* rowp = (unsigned char*)y4 + (size_t)(odd ? dsts[1] : dsts[0]) * 1024 + (c0 - 8 * odd);
; #pragma unroll
;                 for (int bj = 0; bj < 2; ++bj) {
;                     auto r0 = __builtin_amdgcn_permlane16_swap(wq[0][bj][0], wq[1][bj][0], false, false); auto r1 = __builtin_amdgcn_permlane16_swap(wq[0][bj][1], wq[1][bj][1], false, false);
;                     *(GAS u32x4*)(rowp + bj * HALF) = (u32x4){(unsigned)r0[0], (unsigned)r1[0], (unsigned)r0[1], (unsigned)r1[1]}; } }
; template <class Epi, class Sched, bool GATHER, int MODE>
; __device__ __forceinline__ void gemm_phase(PG8_LAS unsigned char* lds, PG8_LAS unsigned* scr, const Gemm g, const Sched& S, const Epi& E, int tid_in) {
;     ...
;         if (!has_next) break;
;         cur = nxt; cA = nA; cB = nB; ++ui;
;         if (GATHER) { const u32x4 nx = gather_read(cur); c0[0] = nx[0]; c0[1] = nx[1]; c1[0] = nx[2]; c1[1] = nx[3]; }
;         if (wr == 1) PG8_BAR;
	v_mul_f32_e32 v38, 0x41800000, v26
	v_pk_fma_f32 v[26:27], v[52:53], v[16:17], v[0:1]
	v_pk_fma_f32 v[54:55], v[54:55], v[18:19], v[2:3]
	v_pk_mul_f32 v[26:27], v[26:27], v[38:39] op_sel_hi:[1,0]
	v_pk_mul_f32 v[52:53], v[54:55], v[38:39] op_sel_hi:[1,0]
	v_med3_f32 v26, v26, s9, v200
	v_med3_f32 v37, v27, s9, v200
	v_mov_b32_e32 v27, v169
	v_cvt_pk_fp8_f32 v27, v26, v37
	v_pk_fma_f32 v[48:49], v[48:49], v[22:23], v[4:5]
	v_med3_f32 v26, v52, s9, v200
	v_med3_f32 v37, v53, s9, v200
	v_pk_mul_f32 v[48:49], v[48:49], v[38:39] op_sel_hi:[1,0]
	v_cvt_pk_fp8_f32 v27, v26, v37 op_sel:[0,0,1]
	v_med3_f32 v37, v48, s9, v200
	v_med3_f32 v39, v49, s9, v200
	v_mov_b32_e32 v26, v169
	v_pk_fma_f32 v[50:51], v[50:51], v[20:21], v[6:7]
	v_cvt_pk_fp8_f32 v26, v37, v39
	v_pk_mul_f32 v[48:49], v[50:51], v[38:39] op_sel_hi:[1,0]
	v_pk_fma_f32 v[50:51], v[78:79], v[28:29], v[10:11]
	v_med3_f32 v37, v48, s9, v200
	v_med3_f32 v39, v49, s9, v200
	v_pk_fma_f32 v[48:49], v[76:77], v[30:31], v[8:9]
	v_cvt_pk_fp8_f32 v26, v37, v39 op_sel:[0,0,1]
	v_pk_mul_f32 v[48:49], v[48:49], v[38:39] op_sel_hi:[1,0]
	v_pk_fma_f32 v[52:53], v[72:73], v[34:35], v[12:13]
	v_med3_f32 v37, v48, s9, v200
	v_med3_f32 v39, v49, s9, v200
	v_mov_b32_e32 v49, v169
	v_cvt_pk_fp8_f32 v49, v37, v39
	v_pk_mul_f32 v[50:51], v[50:51], v[38:39] op_sel_hi:[1,0]
	v_mov_b32_e32 v48, v169
	v_med3_f32 v39, v51, s9, v200
	v_med3_f32 v37, v50, s9, v200
	v_pk_mul_f32 v[52:53], v[52:53], v[38:39] op_sel_hi:[1,0]
	v_cvt_pk_fp8_f32 v49, v37, v39 op_sel:[0,0,1]
	v_med3_f32 v37, v52, s9, v200
	v_med3_f32 v39, v53, s9, v200
	v_cvt_pk_fp8_f32 v48, v37, v39
	ds_read_b32 v39, v36 offset:2752
	v_pk_fma_f32 v[50:51], v[74:75], v[32:33], v[14:15]
	v_pk_fma_f32 v[12:13], v[68:69], v[34:35], v[12:13]
	v_pk_fma_f32 v[8:9], v[64:65], v[30:31], v[8:9]
	v_pk_fma_f32 v[4:5], v[44:45], v[22:23], v[4:5]
	s_waitcnt lgkmcnt(0)
	v_pk_mul_f32 v[36:37], v[50:51], v[38:39] op_sel_hi:[1,0]
	v_pk_fma_f32 v[0:1], v[40:41], v[16:17], v[0:1]
	v_med3_f32 v36, v36, s9, v200
	v_med3_f32 v37, v37, s9, v200
	v_cvt_pk_fp8_f32 v48, v36, v37 op_sel:[0,0,1]
	v_mul_f32_e32 v36, 0x41800000, v39
	v_pk_mul_f32 v[12:13], v[12:13], v[36:37] op_sel_hi:[1,0]
	v_pk_mul_f32 v[8:9], v[8:9], v[36:37] op_sel_hi:[1,0]
	v_pk_mul_f32 v[4:5], v[4:5], v[36:37] op_sel_hi:[1,0]
	v_pk_mul_f32 v[0:1], v[0:1], v[36:37] op_sel_hi:[1,0]
	v_pk_fma_f32 v[10:11], v[66:67], v[28:29], v[10:11]
	v_med3_f32 v12, v12, s9, v200
	v_med3_f32 v8, v8, s9, v200
	v_med3_f32 v13, v13, s9, v200
	v_med3_f32 v9, v9, s9, v200
	v_mov_b32_e32 v50, v169
	v_mov_b32_e32 v51, v169
	v_med3_f32 v4, v4, s9, v200
	v_med3_f32 v0, v0, s9, v200
	v_med3_f32 v5, v5, s9, v200
	v_med3_f32 v1, v1, s9, v200
	v_mov_b32_e32 v28, v169
	v_mov_b32_e32 v29, v169
	v_cvt_pk_fp8_f32 v50, v12, v13
	v_cvt_pk_fp8_f32 v51, v8, v9
	v_cvt_pk_fp8_f32 v28, v4, v5
	v_cvt_pk_fp8_f32 v29, v0, v1
	v_pk_fma_f32 v[14:15], v[70:71], v[32:33], v[14:15]
	v_pk_fma_f32 v[6:7], v[46:47], v[20:21], v[6:7]
	v_pk_fma_f32 v[2:3], v[42:43], v[18:19], v[2:3]
	v_pk_mul_f32 v[14:15], v[14:15], v[36:37] op_sel_hi:[1,0]
	v_pk_mul_f32 v[10:11], v[10:11], v[36:37] op_sel_hi:[1,0]
	v_pk_mul_f32 v[6:7], v[6:7], v[36:37] op_sel_hi:[1,0]
	v_pk_mul_f32 v[2:3], v[2:3], v[36:37] op_sel_hi:[1,0]
	v_med3_f32 v14, v14, s9, v200
	v_med3_f32 v10, v10, s9, v200
	v_med3_f32 v8, v15, s9, v200
	v_med3_f32 v9, v11, s9, v200
	v_med3_f32 v6, v6, s9, v200
	v_med3_f32 v2, v2, s9, v200
	v_med3_f32 v0, v7, s9, v200
	v_med3_f32 v1, v3, s9, v200
	v_cvt_pk_fp8_f32 v50, v14, v8 op_sel:[0,0,1]
	v_cvt_pk_fp8_f32 v51, v10, v9 op_sel:[0,0,1]
	v_cvt_pk_fp8_f32 v28, v6, v0 op_sel:[0,0,1]
	v_cvt_pk_fp8_f32 v29, v2, v1 op_sel:[0,0,1]
	v_cndmask_b32_e32 v0, v25, v24, vcc
	v_ashrrev_i32_e32 v1, 31, v0
	v_lshlrev_b64 v[0:1], 10, v[0:1]
	v_lshl_add_u64 v[0:1], s[30:31], 0, v[0:1]
	v_lshl_add_u64 v[0:1], v[0:1], 0, v[168:169]
	v_permlane16_swap_b32_e32 v48, v50
	v_permlane16_swap_b32_e32 v49, v51
	v_permlane16_swap_b32_e32 v26, v28
	v_permlane16_swap_b32_e32 v27, v29
	s_cmp_eq_u32 s74, s67
	s_mov_b64 s[36:37], -1
	global_store_dwordx4 v[0:1], v[48:51], off
	global_store_dwordx4 v[0:1], v[26:29], off offset:128
	s_cbranch_scc1 .LBB0_944
	s_andn2_b64 vcc, exec, s[14:15]
	s_cbranch_vccnz .LBB0_943
	s_barrier
	s_branch .LBB0_943
